# v38 + combined small edits: P5 expert-scan resume, P0 8x unrolled conversion, MF=9 tail B load moved into last MFMA group, P5 epilogue instruction selection
# speedup vs baseline: 1.0063x; 1.0045x over previous
; DI u32x2 pack4(f32x4 v) { bf16x4_t r = __builtin_convertvector(v, bf16x4_t); return __builtin_bit_cast(u32x2, r); }
; DI int lane_id() { int l; asm volatile("v_mbcnt_lo_u32_b32 %0, -1, 0\n\tv_mbcnt_hi_u32_b32 %0, -1, %0" : "=v"(l)); return l; }
; DI KPtr kargs() { KPtr p = (KPtr)__builtin_amdgcn_kernarg_segment_ptr(); asm volatile("" : "+s"(p)); return p; }
; DI void p0_prologue(const Ctx& c) {
;     const KPtr kp = kargs();
;     const int tid = c.wid * 64 + lane_id();
;     const size_t gt = (size_t)c.bid * NTHR + tid, gs = (size_t)c.G * NTHR;
;     { const f32x4* src = (const f32x4*)kp->in[0]; u32x4* dst = (u32x4*)(c.ws + WS_XB);
;       for (size_t i = gt; i < (size_t)T * D / 8; i += gs) { const f32x4 a = src[2 * i], b = src[2 * i + 1]; const u32x2 lo = pack4(a), hi = pack4(b); dst[i] = (u32x4){lo.x, lo.y, hi.x, hi.y}; } }
.LBB0_5:
	s_or_b64 exec, exec, s[6:7]
	s_mov_b64 s[8:9], s[0:1]
	s_and_b32 s58, s88, 0xffffffc0
	v_mbcnt_lo_u32_b32 v12, -1, 0
	v_mbcnt_hi_u32_b32 v12, -1, v12
	s_ashr_i32 s91, s90, 31
	v_add_u32_e32 v2, s58, v12
	s_lshl_b64 s[4:5], s[90:91], 9
	v_ashrrev_i32_e32 v3, 31, v2
	v_lshl_add_u64 v[0:1], s[4:5], 0, v[2:3]
	s_ashr_i32 s45, s44, 31
	s_mov_b64 s[4:5], 0x200000
	s_lshl_b64 s[6:7], s[44:45], 9
	v_cmp_gt_u64_e32 vcc, s[4:5], v[0:1]
	v_lshlrev_b64 v[4:5], 5, v[2:3]
	s_and_saveexec_b64 s[10:11], vcc
	s_cbranch_execz .LBB0_8
	s_load_dwordx2 s[4:5], s[8:9], 0x0
	s_lshl_b64 s[12:13], s[90:91], 13
	s_add_u32 s12, s34, s12
	s_addc_u32 s13, s35, s13
	v_lshl_add_u64 v[6:7], v[2:3], 4, s[12:13]
	s_mov_b64 s[12:13], 0x10000
	v_lshl_add_u64 v[6:7], v[6:7], 0, s[12:13]
	s_lshl_b64 s[12:13], s[44:45], 13
	s_lshl_b64 s[14:15], s[90:91], 14
	s_waitcnt lgkmcnt(0)
	s_add_u32 s4, s4, s14
	s_addc_u32 s5, s5, s15
	v_lshl_add_u64 v[8:9], s[4:5], 0, v[4:5]
	v_lshl_add_u64 v[8:9], v[8:9], 0, 16
	s_lshl_b64 s[14:15], s[44:45], 14
	s_mov_b64 s[16:17], 0
	s_mov_b64 s[18:19], 0x1fffff
	v_mov_b64_e32 v[10:11], v[0:1]
	s_cmp_lg_u32 s44, 0x100
	s_cbranch_scc1 .LBB0_7
	s_mov_b32 s98, 2
.Lp0_unr:
	v_lshl_add_u64 v[96:97], v[8:9], 0, s[14:15]
	v_lshl_add_u64 v[98:99], v[96:97], 0, s[14:15]
	v_lshl_add_u64 v[100:101], v[98:99], 0, s[14:15]
	v_lshl_add_u64 v[102:103], v[100:101], 0, s[14:15]
	v_lshl_add_u64 v[104:105], v[102:103], 0, s[14:15]
	v_lshl_add_u64 v[106:107], v[104:105], 0, s[14:15]
	v_lshl_add_u64 v[108:109], v[106:107], 0, s[14:15]
	global_load_dwordx4 v[32:35], v[8:9], off offset:-16
	global_load_dwordx4 v[36:39], v[8:9], off
	global_load_dwordx4 v[40:43], v[96:97], off offset:-16
	global_load_dwordx4 v[44:47], v[96:97], off
	global_load_dwordx4 v[48:51], v[98:99], off offset:-16
	global_load_dwordx4 v[52:55], v[98:99], off
	global_load_dwordx4 v[56:59], v[100:101], off offset:-16
	global_load_dwordx4 v[60:63], v[100:101], off
	global_load_dwordx4 v[64:67], v[102:103], off offset:-16
	global_load_dwordx4 v[68:71], v[102:103], off
	global_load_dwordx4 v[72:75], v[104:105], off offset:-16
	global_load_dwordx4 v[76:79], v[104:105], off
	global_load_dwordx4 v[80:83], v[106:107], off offset:-16
	global_load_dwordx4 v[84:87], v[106:107], off
	global_load_dwordx4 v[88:91], v[108:109], off offset:-16
	global_load_dwordx4 v[92:95], v[108:109], off
	v_lshl_add_u64 v[8:9], v[108:109], 0, s[14:15]
	v_lshl_add_u64 v[112:113], v[6:7], 0, s[12:13]
	v_lshl_add_u64 v[114:115], v[112:113], 0, s[12:13]
	v_lshl_add_u64 v[116:117], v[114:115], 0, s[12:13]
	v_lshl_add_u64 v[118:119], v[116:117], 0, s[12:13]
	v_lshl_add_u64 v[120:121], v[118:119], 0, s[12:13]
	v_lshl_add_u64 v[122:123], v[120:121], 0, s[12:13]
	v_lshl_add_u64 v[124:125], v[122:123], 0, s[12:13]
	s_waitcnt vmcnt(14)
	v_cvt_pk_bf16_f32 v128, v32, v33
	v_cvt_pk_bf16_f32 v129, v34, v35
	v_cvt_pk_bf16_f32 v130, v36, v37
	v_cvt_pk_bf16_f32 v131, v38, v39
	global_store_dwordx4 v[6:7], v[128:131], off
	s_waitcnt vmcnt(13)
	v_cvt_pk_bf16_f32 v132, v40, v41
	v_cvt_pk_bf16_f32 v133, v42, v43
	v_cvt_pk_bf16_f32 v134, v44, v45
	v_cvt_pk_bf16_f32 v135, v46, v47
	global_store_dwordx4 v[112:113], v[132:135], off
	s_waitcnt vmcnt(12)
	v_cvt_pk_bf16_f32 v136, v48, v49
	v_cvt_pk_bf16_f32 v137, v50, v51
	v_cvt_pk_bf16_f32 v138, v52, v53
	v_cvt_pk_bf16_f32 v139, v54, v55
	global_store_dwordx4 v[114:115], v[136:139], off
	s_waitcnt vmcnt(11)
	v_cvt_pk_bf16_f32 v140, v56, v57
	v_cvt_pk_bf16_f32 v141, v58, v59
	v_cvt_pk_bf16_f32 v142, v60, v61
	v_cvt_pk_bf16_f32 v143, v62, v63
	global_store_dwordx4 v[116:117], v[140:143], off
	s_waitcnt vmcnt(10)
	v_cvt_pk_bf16_f32 v144, v64, v65
	v_cvt_pk_bf16_f32 v145, v66, v67
	v_cvt_pk_bf16_f32 v146, v68, v69
	v_cvt_pk_bf16_f32 v147, v70, v71
	global_store_dwordx4 v[118:119], v[144:147], off
	s_waitcnt vmcnt(9)
	v_cvt_pk_bf16_f32 v148, v72, v73
	v_cvt_pk_bf16_f32 v149, v74, v75
	v_cvt_pk_bf16_f32 v150, v76, v77
	v_cvt_pk_bf16_f32 v151, v78, v79
	global_store_dwordx4 v[120:121], v[148:151], off
	s_waitcnt vmcnt(8)
	v_cvt_pk_bf16_f32 v152, v80, v81
	v_cvt_pk_bf16_f32 v153, v82, v83
	v_cvt_pk_bf16_f32 v154, v84, v85
	v_cvt_pk_bf16_f32 v155, v86, v87
	global_store_dwordx4 v[122:123], v[152:155], off
	s_waitcnt vmcnt(7)
	v_cvt_pk_bf16_f32 v156, v88, v89
	v_cvt_pk_bf16_f32 v157, v90, v91
	v_cvt_pk_bf16_f32 v158, v92, v93
	v_cvt_pk_bf16_f32 v159, v94, v95
	global_store_dwordx4 v[124:125], v[156:159], off
	v_lshl_add_u64 v[6:7], v[124:125], 0, s[12:13]
	s_sub_i32 s98, s98, 1
	s_cmp_lg_u32 s98, 0
	s_cbranch_scc1 .Lp0_unr
	s_branch .LBB0_8

; #define LAS __attribute__((address_space(3)))
; DI int lane_id() { int l; asm volatile("v_mbcnt_lo_u32_b32 %0, -1, 0\n\tv_mbcnt_hi_u32_b32 %0, -1, %0" : "=v"(l)); return l; }
; #define OPAQUE_LDS(p) asm volatile("" : "+v"(p))
; #define G_SETUP(u) do { G_SETUP_B(u); G_SETUP_A(u); } while (0)
;     ...
;     const int lane = lane_id(), wr = wid >> 2, wc = wid & 3, fr = lane & 15, fq = lane >> 4;
;     U cur;
;     if (!sched.get(0, cur)) return;
;     __amdgpu_buffer_rsrc_t rsB0, rsB1, rsA; unsigned voa0, voa1, voa2, voa3, voa4 = 0;
;     ...
;     G_SETUP(cur);
;     const int hl = lane >> 5, sc = (lane & 31) * 4;
;     const unsigned vob = (unsigned)((2 * wid + hl) * ldb + sc) * 4u;
;     const unsigned kstepB = (unsigned)ldb * 64u;
;     const int pos0 = (GU ? (sc >> 5) * 64 : (sc & ~31)) + ((sc >> 2) & 1) * 16 + ((sc >> 3) & 3) * 4;
;     LAS unsigned char* b_wr = lds + G_BREG + (((2 * wid + hl) ^ (wid & 4)) * G_BSTRIDE) + pos0 * 2; OPAQUE_LDS(b_wr);
;     constexpr int SLAB1 = GU ? 64 : 256;
;     LAS unsigned char* a_rd = lds + G_AREG + wr * (MF * 2048) + ((fr * 64 + fq * 16) ^ (((fr >> 3) & 1) << 5)); OPAQUE_LDS(a_rd);
;     const int q = (lane & 15) >> 2, p = lane & 3;
;     LAS unsigned char* b_rd0 = lds + G_BREG + fq * (8 * G_BSTRIDE) + (((fq & 1) * 4 + q) * G_BSTRIDE) + wc * 128 + p * 8; OPAQUE_LDS(b_rd0);
;     LAS unsigned char* b_rd1 = lds + G_BREG + fq * (8 * G_BSTRIDE) + ((((fq & 1) ^ 1) * 4 + q) * G_BSTRIDE) + wc * 128 + p * 8; OPAQUE_LDS(b_rd1);
.LBB0_646:
	s_andn2_b64 vcc, exec, s[18:19]
	s_cbranch_vccnz .LBB0_664
	s_lshl_b32 s6, s16, 13
	s_ashr_i32 s7, s6, 31
	s_lshl_b32 s18, s17, 10
	s_lshl_b64 s[6:7], s[6:7], 2
	s_add_u32 s66, s74, s6
	s_addc_u32 s67, s75, s7
	s_ashr_i32 s17, s16, 31
	s_lshl_b64 s[6:7], s[16:17], 24
	s_add_u32 s17, s8, s6
	s_mul_i32 s78, s22, 0x120
	s_addc_u32 s22, s9, s7
	s_mul_i32 s100, s72, 0x90
	s_sub_i32 s99, s65, s78
	s_sub_i32 s99, s99, s100
	s_add_i32 s99, s99, 15
	s_max_i32 s99, s99, 0
	s_lshr_b32 s99, s99, 4
	s_min_u32 s99, s99, 9
	s_lshl_b32 s19, s90, 7
	s_and_b32 s76, s19, 0x380
	s_or_b32 s54, s18, s76
	s_ashr_i32 s55, s54, 31
	s_lshl_b64 s[18:19], s[54:55], 2
	s_add_u32 s55, s17, s18
	s_addc_u32 s77, s22, s19
	s_add_u32 s6, s12, s6
	s_addc_u32 s7, s13, s7
	s_add_u32 s79, s6, s18
	s_addc_u32 s80, s7, s19
	s_lshl_b32 s6, s16, 11
	s_ashr_i32 s7, s6, 31
	s_lshl_b64 s[6:7], s[6:7], 2
	s_add_u32 s56, s10, s6
	s_addc_u32 s57, s11, s7
	s_add_u32 s58, s14, s6
	s_addc_u32 s59, s15, s7
	v_mbcnt_lo_u32_b32 v1, -1, 0
	v_mbcnt_hi_u32_b32 v1, -1, v1
	s_lshl_b32 s6, s89, 3
	v_ashrrev_i32_e32 v2, 2, v1
	v_writelane_b32 v242, s92, 8
	s_and_b32 s81, s6, 0x1ffffff0
	v_add_u32_e32 v2, s78, v2
	s_and_b32 s82, s6, 16
	v_writelane_b32 v242, s93, 9
	s_mov_b32 s24, s90
	v_add_u32_e32 v3, s81, v2
	s_add_i32 s7, s65, -1
	s_bitset1_b32 s82, 8
	v_writelane_b32 v242, s24, 10
	s_mov_b32 s19, 0x20000
	s_mov_b32 s18, 0x7ffffff0
	s_waitcnt vmcnt(18)
	v_min_i32_e32 v4, s7, v3
	v_add_u32_e32 v5, 64, v3
	v_add_u32_e32 v6, 0x80, v3
	v_add_u32_e32 v3, 0xc0, v3
	v_add_u32_e32 v2, s82, v2
	v_writelane_b32 v242, s25, 11
	s_and_b32 s25, s67, 0xffff
	s_mov_b32 s24, s66
	s_mov_b32 s26, s18
	s_mov_b32 s27, s19
	v_lshlrev_b32_e32 v4, 2, v4
	v_min_i32_e32 v5, s7, v5
	v_min_i32_e32 v6, s7, v6
	v_min_i32_e32 v3, s7, v3
	v_min_i32_e32 v2, s7, v2
	buffer_load_dword v4, v4, s[24:27], 0 offen
	v_lshlrev_b32_e32 v5, 2, v5
	v_lshlrev_b32_e32 v6, 2, v6
	v_lshlrev_b32_e32 v3, 2, v3
	v_lshlrev_b32_e32 v2, 2, v2
	buffer_load_dword v5, v5, s[24:27], 0 offen
	s_nop 0
	buffer_load_dword v6, v6, s[24:27], 0 offen
	s_nop 0
	buffer_load_dword v3, v3, s[24:27], 0 offen
	s_nop 0
	buffer_load_dword v2, v2, s[24:27], 0 offen
	v_lshlrev_b32_e32 v13, 4, v1
	v_and_b32_e32 v1, 32, v1
	v_bitop3_b32 v1, v13, v1, 48 bitop3:0x6c
	s_and_b32 s84, s88, 64
	s_movk_i32 s83, 0xf000
	v_or_b32_e32 v1, s84, v1
	s_waitcnt vmcnt(22)
	v_and_b32_e32 v8, 15, v0
	v_lshlrev_b32_e32 v10, 2, v0
	s_mul_i32 s22, s72, 0x4800
	s_add_i32 s22, s22, 0
	v_ashrrev_i32_e32 v7, 4, v0
	v_ashrrev_i32_e32 v9, 5, v0
	v_lshlrev_b32_e32 v11, 4, v0
	v_lshl_add_u32 v9, s89, 1, v9
	v_and_b32_e32 v14, 0x1f0, v11
	s_add_i32 s7, 0, 0x12000
	s_movk_i32 s6, 0x220
	v_lshl_or_b32 v184, v9, 13, v14
	v_bitop3_b32 v9, v9, s89, 4 bitop3:0x78
	v_lshlrev_b32_e32 v12, 5, v0
	v_and_b32_e32 v11, 0x180, v11
	v_mul_lo_u32 v9, v9, s6
	v_and_b32_e32 v12, 32, v12
	v_and_b32_e32 v15, 24, v10
	s_and_b32 s21, s21, 0xffff
	v_add3_u32 v9, s7, v9, v11
	s_mov_b32 s40, s20
	s_mov_b32 s42, s18
	s_mov_b32 s43, s19
	s_and_b32 s25, s77, 0xffff
	s_mov_b32 s41, s21
	v_add3_u32 v185, v9, v12, v15
	s_mov_b32 s16, s55
	s_and_b32 s29, s80, 0xffff
	s_mov_b32 s45, s88
	s_mov_b32 s17, s25
	s_mov_b32 s87, 0x40000
	s_mov_b32 s88, 0x60000
	s_mov_b32 s38, s18
	s_mov_b32 s39, s19
	s_mov_b32 s36, s79
	s_mov_b32 s37, s29
	s_mov_b32 s69, s89
	s_add_i32 s68, s5, s78
	s_mov_b32 s24, s55
	s_mov_b32 s23, s19
	s_mov_b32 s28, s79
	s_mov_b32 s92, 0
	s_waitcnt vmcnt(4)
	v_lshlrev_b32_e32 v4, 10, v4
	v_and_or_b32 v189, v4, s83, v1
	s_waitcnt vmcnt(3)
	v_lshlrev_b32_e32 v4, 10, v5
	s_waitcnt vmcnt(2)
	v_lshlrev_b32_e32 v5, 10, v6
	s_waitcnt vmcnt(1)
	v_lshlrev_b32_e32 v3, 10, v3
	s_waitcnt vmcnt(0)
	v_lshlrev_b32_e32 v2, 10, v2
	v_and_or_b32 v192, v4, s83, v1
	v_and_or_b32 v191, v5, s83, v1
	v_and_or_b32 v190, v3, s83, v1
	v_and_or_b32 v193, v2, s83, v1
	v_and_b32_e32 v1, -16, v0
	v_lshl_add_u32 v1, v8, 6, v1
	v_and_b32_e32 v2, 32, v10
	v_xad_u32 v186, v1, v2, s22
	s_movk_i32 s22, 0x1100
	v_bfe_u32 v1, v0, 2, 2
	v_mul_lo_u32 v2, v7, s22
	v_lshlrev_b32_e32 v3, 2, v7
	v_add_u32_e32 v2, s7, v2
	v_and_or_b32 v4, v3, 4, v1
	v_bitop3_b32 v1, v3, 4, v1 bitop3:0x26
	v_mad_u32_u24 v4, v4, s6, v2
	v_lshlrev_b32_e32 v0, 3, v0
	v_mad_u32_u24 v1, v1, s6, v2
	s_lshl_b32 s6, s89, 10
	s_lshl_b32 s7, s73, 7
	v_and_b32_e32 v0, 24, v0
	s_add_i32 s46, s6, 0
	v_add3_u32 v187, v4, s7, v0
	v_add3_u32 v188, v1, s7, v0
	s_mov_b32 m0, s46
	s_barrier
; #define LAS __attribute__((address_space(3)))
; #define G_DMA_A(kt, AO) do { G_DMA1(kt, AO, 0); G_DMA1(kt, AO, 1); G_DMA1(kt, AO, 2); G_DMA1(kt, AO, 3); if (MF == 9) G_DMA5(kt, AO); } while (0)
; #define G_ISSUE_B(kt) do { const unsigned _sb = (unsigned)(kt) * 4u * kstepB; \
;         _Pragma("unroll") for (int _i = 0; _i < 8; ++_i) sb[_i] = bload16(_i < 4 ? rsB0 : rsB1, vob, _sb + (_i & 3) * kstepB); } while (0)
; #define G_WRITE_B(BO) do { \
;         _Pragma("unroll") for (int _i = 0; _i < 8; ++_i) *(LAS u32x2*)(b_wr + (BO) + (_i & 3) * (16 * G_BSTRIDE) + (_i >> 2) * SLAB1) = pack4(__builtin_bit_cast(f32x4, sb[_i])); } while (0)
; #define G_ENDTILE(VM) do { asm volatile("s_waitcnt vmcnt(" #VM ")" ::: "memory"); \
;         asm volatile("s_waitcnt lgkmcnt(0)" ::: "memory"); __builtin_amdgcn_s_barrier(); asm volatile("" ::: "memory"); } while (0)
;     ...
;     __builtin_amdgcn_s_barrier();
;     G_DMA_A(0, G_A0); G_ISSUE_B(0); G_WRITE_B(G_B0);
;     __builtin_amdgcn_sched_barrier(0);
;     G_ISSUE_B(1);
;     __builtin_amdgcn_sched_barrier(0);
;     G_ENDTILE(8);
; DI bool moe_find(const Ctx& c, int qi, int NT, int& e, int& nt, int& mt, int& cn, int& hb) {
;     LAS int* S = (LAS int*)(c.lds + MS_OFF);
;     const int nown = __builtin_amdgcn_readfirstlane(S[0]); int accu = 0;
;     for (int k = 0; k < nown; ++k) { const int mc = __builtin_amdgcn_readfirstlane(S[9 + 4 * k]);
;         if (qi < accu + NT * mc) { const int loc = qi - accu; nt = loc / mc; mt = loc - nt * mc;
;             e = __builtin_amdgcn_readfirstlane(S[8 + 4 * k]); cn = __builtin_amdgcn_readfirstlane(S[10 + 4 * k]); hb = __builtin_amdgcn_readfirstlane(S[11 + 4 * k]); return true; }
;         accu += NT * mc; }
;     return false;
	buffer_load_dwordx4 v189, s[40:43], 0 offen lds
	buffer_load_dwordx4 v[0:3], v184, s[16:19], 0 offen
	buffer_load_dwordx4 v[4:7], v184, s[16:19], s19 offen
	s_add_i32 s86, s46, 0x2000
	buffer_load_dwordx4 v[8:11], v184, s[16:19], s87 offen
	buffer_load_dwordx4 v[12:15], v184, s[16:19], s88 offen
	buffer_load_dwordx4 v[16:19], v184, s[36:39], 0 offen
	s_mov_b32 m0, s86
	s_add_i32 s89, s46, 0x4000
	buffer_load_dwordx4 v[20:23], v184, s[36:39], s19 offen
	buffer_load_dwordx4 v[24:27], v184, s[36:39], s87 offen
	s_lshl_b32 s6, s73, 10
	buffer_load_dwordx4 v192, s[40:43], 0 offen lds
	s_mov_b32 m0, s89
	s_add_i32 s90, s46, 0x6000
	s_add_i32 s48, s6, 0
	buffer_load_dwordx4 v191, s[40:43], 0 offen lds
	s_mov_b32 m0, s90
	buffer_load_dwordx4 v[28:31], v184, s[36:39], s88 offen
	s_add_i32 s91, s48, 0x8000
	buffer_load_dwordx4 v190, s[40:43], 0 offen lds
	s_mov_b32 m0, s91
	s_mov_b32 s22, s18
	buffer_load_dwordx4 v193, s[40:43], 0 offen lds
	s_waitcnt vmcnt(11)
	v_cvt_pk_bf16_f32 v3, v2, v3
	v_cvt_pk_bf16_f32 v2, v0, v1
	s_waitcnt vmcnt(10)
	v_cvt_pk_bf16_f32 v0, v4, v5
	s_waitcnt vmcnt(9)
	v_cvt_pk_bf16_f32 v4, v8, v9
	s_waitcnt vmcnt(7)
	v_cvt_pk_bf16_f32 v9, v18, v19
	v_cvt_pk_bf16_f32 v8, v16, v17
	v_cvt_pk_bf16_f32 v1, v6, v7
	ds_write2_b64 v185, v[2:3], v[8:9] offset1:8
	s_waitcnt vmcnt(6)
	v_cvt_pk_bf16_f32 v3, v22, v23
	v_cvt_pk_bf16_f32 v2, v20, v21
	v_add_u32_e32 v8, 0x2000, v185
	v_cvt_pk_bf16_f32 v5, v10, v11
	ds_write2_b64 v8, v[0:1], v[2:3] offset0:64 offset1:72
	s_waitcnt vmcnt(5)
	v_cvt_pk_bf16_f32 v1, v26, v27
	v_cvt_pk_bf16_f32 v0, v24, v25
	v_add_u32_e32 v2, 0x4000, v185
	v_cvt_pk_bf16_f32 v7, v14, v15
	v_cvt_pk_bf16_f32 v6, v12, v13
	ds_write2_b64 v2, v[4:5], v[0:1] offset0:128 offset1:136
	s_waitcnt vmcnt(2)
	v_cvt_pk_bf16_f32 v1, v30, v31
	v_cvt_pk_bf16_f32 v0, v28, v29
	v_add_u32_e32 v2, 0x6000, v185
	ds_write2_b64 v2, v[6:7], v[0:1] offset0:192 offset1:200
	s_mov_b32 s93, 0x80000
	s_mov_b32 s95, 0xc0000
	s_mov_b32 s94, 0xa0000
	buffer_load_dwordx4 v[12:15], v184, s[16:19], s93 offen
	buffer_load_dwordx4 v[0:3], v184, s[16:19], s94 offen
	s_mov_b32 s96, 0xe0000
	buffer_load_dwordx4 v[28:31], v184, s[16:19], s95 offen
	buffer_load_dwordx4 v[24:27], v184, s[16:19], s96 offen
	buffer_load_dwordx4 v[20:23], v184, s[36:39], s93 offen
	buffer_load_dwordx4 v[4:7], v184, s[36:39], s94 offen
	buffer_load_dwordx4 v[8:11], v184, s[36:39], s95 offen
	buffer_load_dwordx4 v[16:19], v184, s[36:39], s96 offen
	s_waitcnt vmcnt(8)
	s_add_i32 s97, s4, -2
	s_waitcnt lgkmcnt(0)
	s_barrier
	s_cmp_gt_i32 s4, 2
	s_cselect_b64 s[40:41], -1, 0
	s_lshl_b32 s49, s4, 7
	s_add_i32 s85, s46, 0x9000
	s_add_i32 s7, s46, 0xb000
	s_add_i32 s6, s46, 0xd000
	s_add_i32 s47, s46, 0xf000
	s_add_i32 s48, s48, 0x11000
	s_addk_i32 s49, 0xff80
	s_lshl_b32 s4, s73, 5
	s_add_i32 s5, 0, 0x23040
	s_add_i32 s52, 0, 0x2306c
	s_mov_b32 s98, 0x2306c
	s_mov_b32 s101, 0
	s_mov_b32 s53, 0xc0e00000
	v_mov_b32_e32 v194, 0x40e00000
	s_mov_b64 s[30:31], s[22:23]
	s_mov_b64 s[26:27], s[22:23]
	s_branch .LBB0_649

;     ...
;     for (int ui = 0;; ++ui) {
; #pragma unroll
;         for (int m = 0; m < MF; ++m)
; #pragma unroll
;             for (int n = 0; n < 4; ++n) acc[m][n] = (f32x4){0.f, 0.f, 0.f, 0.f};
;         for (int t = 0; t < nt - 2; t += 2) {
;             G_TILE(G_A0, G_B0, true, G_B1, G_A1, t + 1, true, t + 2, (void)0);
.LBB0_649:
	s_andn2_b64 vcc, exec, s[40:41]
	v_mov_b32_e32 v175, 0
	s_cbranch_vccnz .LBB0_652
	s_mov_b32 s16, 0
	s_mov_b32 s17, 0x1e0000
	s_movk_i32 s36, 0x100
	s_cmp_lt_u32 s99, 9
	s_cbranch_scc1 .Lslow_P5
	s_mov_b32 m0, s85
	s_add_i32 s37, s36, 0xffffff80
	ds_read_b64_tr_b16 v[178:179], v188
	ds_read_b64_tr_b16 v[176:177], v187
	ds_read_b64_tr_b16 v[180:181], v187 offset:32
	ds_read_b64_tr_b16 v[198:199], v187 offset:64
	ds_read_b64_tr_b16 v[202:203], v187 offset:96
	ds_read_b128 v[206:209], v186
	ds_read_b64_tr_b16 v[182:183], v188 offset:32
	ds_read_b64_tr_b16 v[200:201], v188 offset:64
	ds_read_b64_tr_b16 v[204:205], v188 offset:96
	ds_read_b128 v[210:213], v186 offset:2048
	ds_read_b128 v[214:217], v186 offset:4096
	buffer_load_dwordx4 v189, s[20:23], s37 offen lds
	s_mov_b32 m0, s7
	s_waitcnt lgkmcnt(5)
	v_mfma_f32_16x16x32_bf16 v[172:175], v[176:179], v[206:209], 0
	buffer_load_dwordx4 v192, s[20:23], s37 offen lds
	s_waitcnt lgkmcnt(4)
	v_mfma_f32_16x16x32_bf16 v[168:171], v[180:183], v[206:209], 0
	s_waitcnt lgkmcnt(3)
	v_mfma_f32_16x16x32_bf16 v[164:167], v[198:201], v[206:209], 0
	s_waitcnt lgkmcnt(2)
	v_mfma_f32_16x16x32_bf16 v[160:163], v[202:205], v[206:209], 0
	s_waitcnt lgkmcnt(1)
	v_mfma_f32_16x16x32_bf16 v[156:159], v[176:179], v[210:213], 0
	s_mov_b32 m0, s6
	s_nop 0
	buffer_load_dwordx4 v191, s[20:23], s37 offen lds
	ds_read_b128 v[206:209], v186 offset:6144
	s_waitcnt vmcnt(10)
	v_cvt_pk_bf16_f32 v15, v14, v15
	v_cvt_pk_bf16_f32 v14, v12, v13
	v_mfma_f32_16x16x32_bf16 v[152:155], v[180:183], v[210:213], 0
	ds_write_b64 v185, v[14:15] offset:34816
	v_mfma_f32_16x16x32_bf16 v[148:151], v[198:201], v[210:213], 0
	s_mov_b32 m0, s47
	s_nop 0
	buffer_load_dwordx4 v190, s[20:23], s37 offen lds
	v_mfma_f32_16x16x32_bf16 v[144:147], v[202:205], v[210:213], 0
	s_waitcnt lgkmcnt(2)
	v_mfma_f32_16x16x32_bf16 v[132:135], v[176:179], v[214:217], 0
	s_mov_b32 m0, s48
	s_nop 0
	buffer_load_dwordx4 v193, s[20:23], s37 offen lds
	s_add_i32 s37, s17, 0xfff20000
	ds_read_b128 v[210:213], v186 offset:8192
	v_mfma_f32_16x16x32_bf16 v[124:127], v[180:183], v[214:217], 0
	v_mfma_f32_16x16x32_bf16 v[120:123], v[198:201], v[214:217], 0
	v_mfma_f32_16x16x32_bf16 v[140:143], v[202:205], v[214:217], 0
	s_waitcnt lgkmcnt(2)
	v_mfma_f32_16x16x32_bf16 v[136:139], v[176:179], v[206:209], 0
	ds_read_b128 v[214:217], v186 offset:10240
	buffer_load_dwordx4 v[12:15], v184, s[24:27], s37 offen
	s_waitcnt vmcnt(12)
	v_cvt_pk_bf16_f32 v3, v2, v3
	v_cvt_pk_bf16_f32 v2, v0, v1
	v_mfma_f32_16x16x32_bf16 v[128:131], v[180:183], v[206:209], 0
	ds_write_b64 v185, v[2:3] offset:43520
	v_mfma_f32_16x16x32_bf16 v[116:119], v[198:201], v[206:209], 0
	v_mfma_f32_16x16x32_bf16 v[112:115], v[202:205], v[206:209], 0
	s_add_i32 s38, s17, 0xfff40000
	s_waitcnt lgkmcnt(2)
	v_mfma_f32_16x16x32_bf16 v[100:103], v[176:179], v[210:213], 0
	ds_read_b128 v[206:209], v186 offset:12288
	v_mfma_f32_16x16x32_bf16 v[92:95], v[180:183], v[210:213], 0
	v_mfma_f32_16x16x32_bf16 v[88:91], v[198:201], v[210:213], 0
	v_mfma_f32_16x16x32_bf16 v[108:111], v[202:205], v[210:213], 0
	s_waitcnt lgkmcnt(2)
	v_mfma_f32_16x16x32_bf16 v[104:107], v[176:179], v[214:217], 0
	ds_read_b128 v[210:213], v186 offset:14336
	buffer_load_dwordx4 v[0:3], v184, s[24:27], s38 offen
	s_waitcnt vmcnt(12)
	v_cvt_pk_bf16_f32 v31, v30, v31
	v_cvt_pk_bf16_f32 v30, v28, v29
	v_mfma_f32_16x16x32_bf16 v[96:99], v[180:183], v[214:217], 0
	ds_write_b64 v185, v[30:31] offset:52224
	v_mfma_f32_16x16x32_bf16 v[84:87], v[198:201], v[214:217], 0
	v_mfma_f32_16x16x32_bf16 v[80:83], v[202:205], v[214:217], 0
	s_add_i32 s39, s17, 0xfff60000
	s_waitcnt lgkmcnt(2)
	v_mfma_f32_16x16x32_bf16 v[72:75], v[176:179], v[206:209], 0
	ds_read_b128 v[214:217], v186 offset:16384
	v_mfma_f32_16x16x32_bf16 v[64:67], v[180:183], v[206:209], 0
	v_mfma_f32_16x16x32_bf16 v[60:63], v[198:201], v[206:209], 0
	v_mfma_f32_16x16x32_bf16 v[76:79], v[202:205], v[206:209], 0
	s_waitcnt lgkmcnt(2)
	v_mfma_f32_16x16x32_bf16 v[68:71], v[176:179], v[210:213], 0
	ds_read_b128 v[206:209], v186 offset:1024
	buffer_load_dwordx4 v[28:31], v184, s[24:27], s39 offen
	s_waitcnt vmcnt(12)
	v_cvt_pk_bf16_f32 v27, v26, v27
	v_cvt_pk_bf16_f32 v26, v24, v25
	v_mfma_f32_16x16x32_bf16 v[56:59], v[180:183], v[210:213], 0
	ds_write_b64 v185, v[26:27] offset:60928
	v_mfma_f32_16x16x32_bf16 v[52:55], v[198:201], v[210:213], 0
	v_mfma_f32_16x16x32_bf16 v[48:51], v[202:205], v[210:213], 0
	s_add_i32 s42, s17, 0xfff80000
	ds_read_b128 v[210:213], v186 offset:3072
	s_waitcnt lgkmcnt(3)
	v_mfma_f32_16x16x32_bf16 v[44:47], v[176:179], v[214:217], 0
	ds_read_b64_tr_b16 v[246:247], v188 offset:17408
	ds_read_b64_tr_b16 v[220:221], v188 offset:17440
	ds_read_b64_tr_b16 v[244:245], v187 offset:17408
	ds_read_b64_tr_b16 v[218:219], v187 offset:17440
	v_mfma_f32_16x16x32_bf16 v[40:43], v[180:183], v[214:217], 0
	ds_read_b64_tr_b16 v[248:249], v187 offset:17472
	ds_read_b64_tr_b16 v[250:251], v188 offset:17472
	v_mfma_f32_16x16x32_bf16 v[36:39], v[198:201], v[214:217], 0
	ds_read_b64_tr_b16 v[252:253], v187 offset:17504
	ds_read_b64_tr_b16 v[254:255], v188 offset:17504
	v_mfma_f32_16x16x32_bf16 v[32:35], v[202:205], v[214:217], 0
	s_waitcnt lgkmcnt(5)
	v_mfma_f32_16x16x32_bf16 v[172:175], v[244:247], v[206:209], v[172:175]
	ds_read_b128 v[202:205], v186 offset:5120
	buffer_load_dwordx4 v[24:27], v184, s[24:27], s42 offen
	s_waitcnt vmcnt(12)
	v_cvt_pk_bf16_f32 v23, v22, v23
	v_cvt_pk_bf16_f32 v22, v20, v21
	s_waitcnt lgkmcnt(5)
	v_mfma_f32_16x16x32_bf16 v[168:171], v[218:221], v[206:209], v[168:171]
	ds_write_b64 v185, v[22:23] offset:34880
	s_waitcnt lgkmcnt(4)
	v_mfma_f32_16x16x32_bf16 v[164:167], v[248:251], v[206:209], v[164:167]
	s_waitcnt lgkmcnt(2)
	v_mfma_f32_16x16x32_bf16 v[160:163], v[252:255], v[206:209], v[160:163]
	v_mfma_f32_16x16x32_bf16 v[156:159], v[244:247], v[210:213], v[156:159]
	ds_read_b128 v[206:209], v186 offset:7168
	v_mfma_f32_16x16x32_bf16 v[152:155], v[218:221], v[210:213], v[152:155]
	v_mfma_f32_16x16x32_bf16 v[148:151], v[248:251], v[210:213], v[148:151]
	v_mfma_f32_16x16x32_bf16 v[144:147], v[252:255], v[210:213], v[144:147]
	s_waitcnt lgkmcnt(2)
	v_mfma_f32_16x16x32_bf16 v[132:135], v[244:247], v[202:205], v[132:135]
	ds_read_b128 v[210:213], v186 offset:9216
	buffer_load_dwordx4 v[20:23], v184, s[28:31], s37 offen
	s_waitcnt vmcnt(12)
	v_cvt_pk_bf16_f32 v7, v6, v7
	v_cvt_pk_bf16_f32 v6, v4, v5
	v_mfma_f32_16x16x32_bf16 v[124:127], v[218:221], v[202:205], v[124:127]
	ds_write_b64 v185, v[6:7] offset:43584
	v_mfma_f32_16x16x32_bf16 v[120:123], v[248:251], v[202:205], v[120:123]
	v_mfma_f32_16x16x32_bf16 v[140:143], v[252:255], v[202:205], v[140:143]
	s_waitcnt lgkmcnt(2)
	v_mfma_f32_16x16x32_bf16 v[136:139], v[244:247], v[206:209], v[136:139]
	ds_read_b128 v[202:205], v186 offset:11264
	v_mfma_f32_16x16x32_bf16 v[128:131], v[218:221], v[206:209], v[128:131]
	v_mfma_f32_16x16x32_bf16 v[116:119], v[248:251], v[206:209], v[116:119]
	v_mfma_f32_16x16x32_bf16 v[112:115], v[252:255], v[206:209], v[112:115]
	s_waitcnt lgkmcnt(2)
	v_mfma_f32_16x16x32_bf16 v[100:103], v[244:247], v[210:213], v[100:103]
	ds_read_b128 v[206:209], v186 offset:13312
	buffer_load_dwordx4 v[4:7], v184, s[28:31], s38 offen
	s_waitcnt vmcnt(12)
	v_cvt_pk_bf16_f32 v11, v10, v11
	v_cvt_pk_bf16_f32 v10, v8, v9
	v_mfma_f32_16x16x32_bf16 v[92:95], v[218:221], v[210:213], v[92:95]
	ds_write_b64 v185, v[10:11] offset:52288
	v_mfma_f32_16x16x32_bf16 v[88:91], v[248:251], v[210:213], v[88:91]
	v_mfma_f32_16x16x32_bf16 v[108:111], v[252:255], v[210:213], v[108:111]
	s_waitcnt lgkmcnt(2)
	v_mfma_f32_16x16x32_bf16 v[104:107], v[244:247], v[202:205], v[104:107]
	ds_read_b128 v[210:213], v186 offset:15360
	v_mfma_f32_16x16x32_bf16 v[96:99], v[218:221], v[202:205], v[96:99]
	v_mfma_f32_16x16x32_bf16 v[84:87], v[248:251], v[202:205], v[84:87]
	v_mfma_f32_16x16x32_bf16 v[80:83], v[252:255], v[202:205], v[80:83]
	s_waitcnt lgkmcnt(2)
	v_mfma_f32_16x16x32_bf16 v[72:75], v[244:247], v[206:209], v[72:75]
	ds_read_b128 v[238:241], v186 offset:17408
	buffer_load_dwordx4 v[8:11], v184, s[28:31], s39 offen
	s_waitcnt vmcnt(12)
	v_cvt_pk_bf16_f32 v19, v18, v19
	v_cvt_pk_bf16_f32 v18, v16, v17
	v_mfma_f32_16x16x32_bf16 v[64:67], v[218:221], v[206:209], v[64:67]
	ds_write_b64 v185, v[18:19] offset:60992
	v_mfma_f32_16x16x32_bf16 v[60:63], v[248:251], v[206:209], v[60:63]
	v_mfma_f32_16x16x32_bf16 v[76:79], v[252:255], v[206:209], v[76:79]
	s_waitcnt lgkmcnt(2)
	v_mfma_f32_16x16x32_bf16 v[68:71], v[244:247], v[210:213], v[68:71]
	buffer_load_dwordx4 v[16:19], v184, s[28:31], s42 offen
	v_mfma_f32_16x16x32_bf16 v[56:59], v[218:221], v[210:213], v[56:59]
	v_mfma_f32_16x16x32_bf16 v[52:55], v[248:251], v[210:213], v[52:55]
	v_mfma_f32_16x16x32_bf16 v[48:51], v[252:255], v[210:213], v[48:51]
	s_waitcnt lgkmcnt(1)
	s_waitcnt vmcnt(8)
	s_mov_b32 m0, s46
	s_waitcnt lgkmcnt(0)
	s_barrier
	ds_read_b64_tr_b16 v[178:179], v188 offset:34816
	ds_read_b64_tr_b16 v[176:177], v187 offset:34816
	ds_read_b64_tr_b16 v[180:181], v187 offset:34848
	ds_read_b64_tr_b16 v[198:199], v187 offset:34880
	ds_read_b64_tr_b16 v[202:203], v187 offset:34912
	ds_read_b128 v[206:209], v186 offset:36864
	ds_read_b64_tr_b16 v[182:183], v188 offset:34848
	ds_read_b64_tr_b16 v[200:201], v188 offset:34880
	ds_read_b64_tr_b16 v[204:205], v188 offset:34912
	ds_read_b128 v[210:213], v186 offset:38912
	ds_read_b128 v[214:217], v186 offset:40960
	buffer_load_dwordx4 v189, s[20:23], s36 offen lds
	s_mov_b32 m0, s86
	v_mfma_f32_16x16x32_bf16 v[44:47], v[244:247], v[238:241], v[44:47]
	v_mfma_f32_16x16x32_bf16 v[40:43], v[218:221], v[238:241], v[40:43]
	v_mfma_f32_16x16x32_bf16 v[36:39], v[248:251], v[238:241], v[36:39]
	v_mfma_f32_16x16x32_bf16 v[32:35], v[252:255], v[238:241], v[32:35]
	s_waitcnt lgkmcnt(5)
	v_mfma_f32_16x16x32_bf16 v[172:175], v[176:179], v[206:209], v[172:175]
	buffer_load_dwordx4 v192, s[20:23], s36 offen lds
	s_add_i32 s37, s17, 0xfffa0000
	s_waitcnt lgkmcnt(4)
	v_mfma_f32_16x16x32_bf16 v[168:171], v[180:183], v[206:209], v[168:171]
	s_waitcnt lgkmcnt(3)
	v_mfma_f32_16x16x32_bf16 v[164:167], v[198:201], v[206:209], v[164:167]
	s_waitcnt lgkmcnt(2)
	v_mfma_f32_16x16x32_bf16 v[160:163], v[202:205], v[206:209], v[160:163]
	s_waitcnt lgkmcnt(1)
	v_mfma_f32_16x16x32_bf16 v[156:159], v[176:179], v[210:213], v[156:159]
	s_mov_b32 m0, s89
	s_nop 0
	buffer_load_dwordx4 v191, s[20:23], s36 offen lds
	ds_read_b128 v[206:209], v186 offset:43008
	s_waitcnt vmcnt(10)
	v_cvt_pk_bf16_f32 v15, v14, v15
	v_cvt_pk_bf16_f32 v14, v12, v13
	v_mfma_f32_16x16x32_bf16 v[152:155], v[180:183], v[210:213], v[152:155]
	ds_write_b64 v185, v[14:15]
	v_mfma_f32_16x16x32_bf16 v[148:151], v[198:201], v[210:213], v[148:151]
	s_mov_b32 m0, s90
	s_nop 0
	buffer_load_dwordx4 v190, s[20:23], s36 offen lds
	v_mfma_f32_16x16x32_bf16 v[144:147], v[202:205], v[210:213], v[144:147]
	s_waitcnt lgkmcnt(2)
	v_mfma_f32_16x16x32_bf16 v[132:135], v[176:179], v[214:217], v[132:135]
	s_mov_b32 m0, s91
	s_nop 0
	buffer_load_dwordx4 v193, s[20:23], s36 offen lds
	ds_read_b128 v[210:213], v186 offset:45056
	v_mfma_f32_16x16x32_bf16 v[124:127], v[180:183], v[214:217], v[124:127]
	v_mfma_f32_16x16x32_bf16 v[120:123], v[198:201], v[214:217], v[120:123]
	v_mfma_f32_16x16x32_bf16 v[140:143], v[202:205], v[214:217], v[140:143]
	s_waitcnt lgkmcnt(2)
; #define G_ENDTILE(VM) do { asm volatile("s_waitcnt vmcnt(" #VM ")" ::: "memory"); \
;         asm volatile("s_waitcnt lgkmcnt(0)" ::: "memory"); __builtin_amdgcn_s_barrier(); asm volatile("" ::: "memory"); } while (0)
;     ...
;         for (int t = 0; t < nt - 2; t += 2) {
;             G_TILE(G_A0, G_B0, true, G_B1, G_A1, t + 1, true, t + 2, (void)0);
;             G_ENDTILE(8);
;             G_TILE(G_A1, G_B1, true, G_B0, G_A0, t + 2, true, t + 3, (void)0);
;             G_ENDTILE(8);
;         }
	v_mfma_f32_16x16x32_bf16 v[136:139], v[176:179], v[206:209], v[136:139]
	ds_read_b128 v[214:217], v186 offset:47104
	buffer_load_dwordx4 v[12:15], v184, s[24:27], s37 offen
	s_waitcnt vmcnt(12)
	v_cvt_pk_bf16_f32 v3, v2, v3
	v_cvt_pk_bf16_f32 v2, v0, v1
	v_mfma_f32_16x16x32_bf16 v[128:131], v[180:183], v[206:209], v[128:131]
	ds_write_b64 v185, v[2:3] offset:8704
	v_mfma_f32_16x16x32_bf16 v[116:119], v[198:201], v[206:209], v[116:119]
	v_mfma_f32_16x16x32_bf16 v[112:115], v[202:205], v[206:209], v[112:115]
	s_add_i32 s38, s17, 0xfffc0000
	s_waitcnt lgkmcnt(2)
	v_mfma_f32_16x16x32_bf16 v[100:103], v[176:179], v[210:213], v[100:103]
	ds_read_b128 v[206:209], v186 offset:49152
	v_mfma_f32_16x16x32_bf16 v[92:95], v[180:183], v[210:213], v[92:95]
	v_mfma_f32_16x16x32_bf16 v[88:91], v[198:201], v[210:213], v[88:91]
	v_mfma_f32_16x16x32_bf16 v[108:111], v[202:205], v[210:213], v[108:111]
	s_waitcnt lgkmcnt(2)
	v_mfma_f32_16x16x32_bf16 v[104:107], v[176:179], v[214:217], v[104:107]
	ds_read_b128 v[210:213], v186 offset:51200
	buffer_load_dwordx4 v[0:3], v184, s[24:27], s38 offen
	s_waitcnt vmcnt(12)
	v_cvt_pk_bf16_f32 v31, v30, v31
	v_cvt_pk_bf16_f32 v30, v28, v29
	v_mfma_f32_16x16x32_bf16 v[96:99], v[180:183], v[214:217], v[96:99]
	ds_write_b64 v185, v[30:31] offset:17408
	v_mfma_f32_16x16x32_bf16 v[84:87], v[198:201], v[214:217], v[84:87]
	v_mfma_f32_16x16x32_bf16 v[80:83], v[202:205], v[214:217], v[80:83]
	s_add_i32 s39, s17, 0xfffe0000
	s_waitcnt lgkmcnt(2)
	v_mfma_f32_16x16x32_bf16 v[72:75], v[176:179], v[206:209], v[72:75]
	ds_read_b128 v[214:217], v186 offset:53248
	v_mfma_f32_16x16x32_bf16 v[64:67], v[180:183], v[206:209], v[64:67]
	v_mfma_f32_16x16x32_bf16 v[60:63], v[198:201], v[206:209], v[60:63]
	v_mfma_f32_16x16x32_bf16 v[76:79], v[202:205], v[206:209], v[76:79]
	s_waitcnt lgkmcnt(2)
	v_mfma_f32_16x16x32_bf16 v[68:71], v[176:179], v[210:213], v[68:71]
	ds_read_b128 v[206:209], v186 offset:37888
	buffer_load_dwordx4 v[28:31], v184, s[24:27], s39 offen
	s_waitcnt vmcnt(12)
	v_cvt_pk_bf16_f32 v27, v26, v27
	v_cvt_pk_bf16_f32 v26, v24, v25
	v_mfma_f32_16x16x32_bf16 v[56:59], v[180:183], v[210:213], v[56:59]
	ds_write_b64 v185, v[26:27] offset:26112
	v_mfma_f32_16x16x32_bf16 v[52:55], v[198:201], v[210:213], v[52:55]
	v_mfma_f32_16x16x32_bf16 v[48:51], v[202:205], v[210:213], v[48:51]
	ds_read_b128 v[210:213], v186 offset:39936
	s_waitcnt lgkmcnt(3)
	v_mfma_f32_16x16x32_bf16 v[44:47], v[176:179], v[214:217], v[44:47]
	ds_read_b64_tr_b16 v[246:247], v188 offset:52224
	ds_read_b64_tr_b16 v[220:221], v188 offset:52256
	ds_read_b64_tr_b16 v[244:245], v187 offset:52224
	ds_read_b64_tr_b16 v[218:219], v187 offset:52256
	v_mfma_f32_16x16x32_bf16 v[40:43], v[180:183], v[214:217], v[40:43]
	ds_read_b64_tr_b16 v[248:249], v187 offset:52288
	ds_read_b64_tr_b16 v[250:251], v188 offset:52288
	v_mfma_f32_16x16x32_bf16 v[36:39], v[198:201], v[214:217], v[36:39]
	ds_read_b64_tr_b16 v[252:253], v187 offset:52320
	ds_read_b64_tr_b16 v[254:255], v188 offset:52320
	v_mfma_f32_16x16x32_bf16 v[32:35], v[202:205], v[214:217], v[32:35]
	s_waitcnt lgkmcnt(5)
	v_mfma_f32_16x16x32_bf16 v[172:175], v[244:247], v[206:209], v[172:175]
	ds_read_b128 v[202:205], v186 offset:41984
	buffer_load_dwordx4 v[24:27], v184, s[24:27], s17 offen
	s_waitcnt vmcnt(12)
	v_cvt_pk_bf16_f32 v23, v22, v23
	v_cvt_pk_bf16_f32 v22, v20, v21
	s_waitcnt lgkmcnt(5)
	v_mfma_f32_16x16x32_bf16 v[168:171], v[218:221], v[206:209], v[168:171]
	ds_write_b64 v185, v[22:23] offset:64
	s_waitcnt lgkmcnt(4)
	v_mfma_f32_16x16x32_bf16 v[164:167], v[248:251], v[206:209], v[164:167]
	s_waitcnt lgkmcnt(2)
	v_mfma_f32_16x16x32_bf16 v[160:163], v[252:255], v[206:209], v[160:163]
	v_mfma_f32_16x16x32_bf16 v[156:159], v[244:247], v[210:213], v[156:159]
	ds_read_b128 v[206:209], v186 offset:44032
	v_mfma_f32_16x16x32_bf16 v[152:155], v[218:221], v[210:213], v[152:155]
	v_mfma_f32_16x16x32_bf16 v[148:151], v[248:251], v[210:213], v[148:151]
	v_mfma_f32_16x16x32_bf16 v[144:147], v[252:255], v[210:213], v[144:147]
	s_waitcnt lgkmcnt(2)
	v_mfma_f32_16x16x32_bf16 v[132:135], v[244:247], v[202:205], v[132:135]
	ds_read_b128 v[210:213], v186 offset:46080
	buffer_load_dwordx4 v[20:23], v184, s[28:31], s37 offen
	s_waitcnt vmcnt(12)
	v_cvt_pk_bf16_f32 v7, v6, v7
	v_cvt_pk_bf16_f32 v6, v4, v5
	v_mfma_f32_16x16x32_bf16 v[124:127], v[218:221], v[202:205], v[124:127]
	ds_write_b64 v185, v[6:7] offset:8768
	v_mfma_f32_16x16x32_bf16 v[120:123], v[248:251], v[202:205], v[120:123]
	v_mfma_f32_16x16x32_bf16 v[140:143], v[252:255], v[202:205], v[140:143]
	s_waitcnt lgkmcnt(2)
	v_mfma_f32_16x16x32_bf16 v[136:139], v[244:247], v[206:209], v[136:139]
	ds_read_b128 v[202:205], v186 offset:48128
	v_mfma_f32_16x16x32_bf16 v[128:131], v[218:221], v[206:209], v[128:131]
	v_mfma_f32_16x16x32_bf16 v[116:119], v[248:251], v[206:209], v[116:119]
	v_mfma_f32_16x16x32_bf16 v[112:115], v[252:255], v[206:209], v[112:115]
	s_waitcnt lgkmcnt(2)
	v_mfma_f32_16x16x32_bf16 v[100:103], v[244:247], v[210:213], v[100:103]
	ds_read_b128 v[206:209], v186 offset:50176
	buffer_load_dwordx4 v[4:7], v184, s[28:31], s38 offen
	s_waitcnt vmcnt(12)
	v_cvt_pk_bf16_f32 v11, v10, v11
	v_cvt_pk_bf16_f32 v10, v8, v9
	v_mfma_f32_16x16x32_bf16 v[92:95], v[218:221], v[210:213], v[92:95]
	ds_write_b64 v185, v[10:11] offset:17472
	v_mfma_f32_16x16x32_bf16 v[88:91], v[248:251], v[210:213], v[88:91]
	v_mfma_f32_16x16x32_bf16 v[108:111], v[252:255], v[210:213], v[108:111]
	s_waitcnt lgkmcnt(2)
	v_mfma_f32_16x16x32_bf16 v[104:107], v[244:247], v[202:205], v[104:107]
	ds_read_b128 v[210:213], v186 offset:52224
	v_mfma_f32_16x16x32_bf16 v[96:99], v[218:221], v[202:205], v[96:99]
	v_mfma_f32_16x16x32_bf16 v[84:87], v[248:251], v[202:205], v[84:87]
	v_mfma_f32_16x16x32_bf16 v[80:83], v[252:255], v[202:205], v[80:83]
	s_waitcnt lgkmcnt(2)
	v_mfma_f32_16x16x32_bf16 v[72:75], v[244:247], v[206:209], v[72:75]
	ds_read_b128 v[238:241], v186 offset:54272
	buffer_load_dwordx4 v[8:11], v184, s[28:31], s39 offen
	s_waitcnt vmcnt(12)
	v_cvt_pk_bf16_f32 v19, v18, v19
	v_cvt_pk_bf16_f32 v18, v16, v17
	v_mfma_f32_16x16x32_bf16 v[64:67], v[218:221], v[206:209], v[64:67]
	ds_write_b64 v185, v[18:19] offset:26176
	v_mfma_f32_16x16x32_bf16 v[60:63], v[248:251], v[206:209], v[60:63]
	v_mfma_f32_16x16x32_bf16 v[76:79], v[252:255], v[206:209], v[76:79]
	s_waitcnt lgkmcnt(2)
	v_mfma_f32_16x16x32_bf16 v[68:71], v[244:247], v[210:213], v[68:71]
	buffer_load_dwordx4 v[16:19], v184, s[28:31], s17 offen
	v_mfma_f32_16x16x32_bf16 v[56:59], v[218:221], v[210:213], v[56:59]
	v_mfma_f32_16x16x32_bf16 v[52:55], v[248:251], v[210:213], v[52:55]
	v_mfma_f32_16x16x32_bf16 v[48:51], v[252:255], v[210:213], v[48:51]
	s_waitcnt lgkmcnt(1)
	s_waitcnt vmcnt(8)
	s_waitcnt lgkmcnt(0)
	s_barrier
	s_add_i32 s16, s16, 2
	s_add_i32 s17, s17, 0x100000
	s_addk_i32 s36, 0x100
	s_cmp_ge_i32 s16, s97
	s_cbranch_scc1 .Lflush_P5
;     ...
;         for (int t = 0; t < nt - 2; t += 2) {
;             G_TILE(G_A0, G_B0, true, G_B1, G_A1, t + 1, true, t + 2, (void)0);
.LBB0_651:
	s_mov_b32 m0, s85
	s_add_i32 s37, s36, 0xffffff80
	ds_read_b64_tr_b16 v[178:179], v188
	ds_read_b64_tr_b16 v[176:177], v187
	ds_read_b64_tr_b16 v[180:181], v187 offset:32
	ds_read_b64_tr_b16 v[198:199], v187 offset:64
	ds_read_b64_tr_b16 v[202:203], v187 offset:96
	ds_read_b128 v[206:209], v186
	ds_read_b64_tr_b16 v[182:183], v188 offset:32
	ds_read_b64_tr_b16 v[200:201], v188 offset:64
	ds_read_b64_tr_b16 v[204:205], v188 offset:96
	ds_read_b128 v[210:213], v186 offset:2048
	ds_read_b128 v[214:217], v186 offset:4096
	buffer_load_dwordx4 v189, s[20:23], s37 offen lds
	s_mov_b32 m0, s7
	v_mfma_f32_16x16x32_bf16 v[44:47], v[244:247], v[238:241], v[44:47]
	v_mfma_f32_16x16x32_bf16 v[40:43], v[218:221], v[238:241], v[40:43]
	v_mfma_f32_16x16x32_bf16 v[36:39], v[248:251], v[238:241], v[36:39]
	v_mfma_f32_16x16x32_bf16 v[32:35], v[252:255], v[238:241], v[32:35]
	s_waitcnt lgkmcnt(5)
	v_mfma_f32_16x16x32_bf16 v[172:175], v[176:179], v[206:209], v[172:175]
	buffer_load_dwordx4 v192, s[20:23], s37 offen lds
	s_waitcnt lgkmcnt(4)
	v_mfma_f32_16x16x32_bf16 v[168:171], v[180:183], v[206:209], v[168:171]
	s_waitcnt lgkmcnt(3)
	v_mfma_f32_16x16x32_bf16 v[164:167], v[198:201], v[206:209], v[164:167]
	s_waitcnt lgkmcnt(2)
	v_mfma_f32_16x16x32_bf16 v[160:163], v[202:205], v[206:209], v[160:163]
	s_waitcnt lgkmcnt(1)
	v_mfma_f32_16x16x32_bf16 v[156:159], v[176:179], v[210:213], v[156:159]
	s_mov_b32 m0, s6
	s_nop 0
	buffer_load_dwordx4 v191, s[20:23], s37 offen lds
	ds_read_b128 v[206:209], v186 offset:6144
	s_waitcnt vmcnt(10)
	v_cvt_pk_bf16_f32 v15, v14, v15
	v_cvt_pk_bf16_f32 v14, v12, v13
	v_mfma_f32_16x16x32_bf16 v[152:155], v[180:183], v[210:213], v[152:155]
	ds_write_b64 v185, v[14:15] offset:34816
	v_mfma_f32_16x16x32_bf16 v[148:151], v[198:201], v[210:213], v[148:151]
	s_mov_b32 m0, s47
	s_nop 0
	buffer_load_dwordx4 v190, s[20:23], s37 offen lds
	v_mfma_f32_16x16x32_bf16 v[144:147], v[202:205], v[210:213], v[144:147]
	s_waitcnt lgkmcnt(2)
	v_mfma_f32_16x16x32_bf16 v[132:135], v[176:179], v[214:217], v[132:135]
	s_mov_b32 m0, s48
	s_nop 0
	buffer_load_dwordx4 v193, s[20:23], s37 offen lds
	s_add_i32 s37, s17, 0xfff20000
	ds_read_b128 v[210:213], v186 offset:8192
	v_mfma_f32_16x16x32_bf16 v[124:127], v[180:183], v[214:217], v[124:127]
	v_mfma_f32_16x16x32_bf16 v[120:123], v[198:201], v[214:217], v[120:123]
	v_mfma_f32_16x16x32_bf16 v[140:143], v[202:205], v[214:217], v[140:143]
	s_waitcnt lgkmcnt(2)
	v_mfma_f32_16x16x32_bf16 v[136:139], v[176:179], v[206:209], v[136:139]
	ds_read_b128 v[214:217], v186 offset:10240
	buffer_load_dwordx4 v[12:15], v184, s[24:27], s37 offen
	s_waitcnt vmcnt(12)
	v_cvt_pk_bf16_f32 v3, v2, v3
	v_cvt_pk_bf16_f32 v2, v0, v1
	v_mfma_f32_16x16x32_bf16 v[128:131], v[180:183], v[206:209], v[128:131]
	ds_write_b64 v185, v[2:3] offset:43520
	v_mfma_f32_16x16x32_bf16 v[116:119], v[198:201], v[206:209], v[116:119]
	v_mfma_f32_16x16x32_bf16 v[112:115], v[202:205], v[206:209], v[112:115]
	s_add_i32 s38, s17, 0xfff40000
	s_waitcnt lgkmcnt(2)
	v_mfma_f32_16x16x32_bf16 v[100:103], v[176:179], v[210:213], v[100:103]
	ds_read_b128 v[206:209], v186 offset:12288
	v_mfma_f32_16x16x32_bf16 v[92:95], v[180:183], v[210:213], v[92:95]
	v_mfma_f32_16x16x32_bf16 v[88:91], v[198:201], v[210:213], v[88:91]
	v_mfma_f32_16x16x32_bf16 v[108:111], v[202:205], v[210:213], v[108:111]
	s_waitcnt lgkmcnt(2)
	v_mfma_f32_16x16x32_bf16 v[104:107], v[176:179], v[214:217], v[104:107]
	ds_read_b128 v[210:213], v186 offset:14336
	buffer_load_dwordx4 v[0:3], v184, s[24:27], s38 offen
	s_waitcnt vmcnt(12)
	v_cvt_pk_bf16_f32 v31, v30, v31
	v_cvt_pk_bf16_f32 v30, v28, v29
	v_mfma_f32_16x16x32_bf16 v[96:99], v[180:183], v[214:217], v[96:99]
	ds_write_b64 v185, v[30:31] offset:52224
	v_mfma_f32_16x16x32_bf16 v[84:87], v[198:201], v[214:217], v[84:87]
	v_mfma_f32_16x16x32_bf16 v[80:83], v[202:205], v[214:217], v[80:83]
	s_add_i32 s39, s17, 0xfff60000
	s_waitcnt lgkmcnt(2)
	v_mfma_f32_16x16x32_bf16 v[72:75], v[176:179], v[206:209], v[72:75]
	ds_read_b128 v[214:217], v186 offset:16384
	v_mfma_f32_16x16x32_bf16 v[64:67], v[180:183], v[206:209], v[64:67]
	v_mfma_f32_16x16x32_bf16 v[60:63], v[198:201], v[206:209], v[60:63]
	v_mfma_f32_16x16x32_bf16 v[76:79], v[202:205], v[206:209], v[76:79]
	s_waitcnt lgkmcnt(2)
	v_mfma_f32_16x16x32_bf16 v[68:71], v[176:179], v[210:213], v[68:71]
	ds_read_b128 v[206:209], v186 offset:1024
	buffer_load_dwordx4 v[28:31], v184, s[24:27], s39 offen
	s_waitcnt vmcnt(12)
	v_cvt_pk_bf16_f32 v27, v26, v27
	v_cvt_pk_bf16_f32 v26, v24, v25
	v_mfma_f32_16x16x32_bf16 v[56:59], v[180:183], v[210:213], v[56:59]
	ds_write_b64 v185, v[26:27] offset:60928
	v_mfma_f32_16x16x32_bf16 v[52:55], v[198:201], v[210:213], v[52:55]
	v_mfma_f32_16x16x32_bf16 v[48:51], v[202:205], v[210:213], v[48:51]
	s_add_i32 s42, s17, 0xfff80000
	ds_read_b128 v[210:213], v186 offset:3072
	s_waitcnt lgkmcnt(3)
	v_mfma_f32_16x16x32_bf16 v[44:47], v[176:179], v[214:217], v[44:47]
	ds_read_b64_tr_b16 v[246:247], v188 offset:17408
	ds_read_b64_tr_b16 v[220:221], v188 offset:17440
	ds_read_b64_tr_b16 v[244:245], v187 offset:17408
	ds_read_b64_tr_b16 v[218:219], v187 offset:17440
	v_mfma_f32_16x16x32_bf16 v[40:43], v[180:183], v[214:217], v[40:43]
	ds_read_b64_tr_b16 v[248:249], v187 offset:17472
	ds_read_b64_tr_b16 v[250:251], v188 offset:17472
	v_mfma_f32_16x16x32_bf16 v[36:39], v[198:201], v[214:217], v[36:39]
	ds_read_b64_tr_b16 v[252:253], v187 offset:17504
	ds_read_b64_tr_b16 v[254:255], v188 offset:17504
	v_mfma_f32_16x16x32_bf16 v[32:35], v[202:205], v[214:217], v[32:35]
	s_waitcnt lgkmcnt(5)
	v_mfma_f32_16x16x32_bf16 v[172:175], v[244:247], v[206:209], v[172:175]
	ds_read_b128 v[202:205], v186 offset:5120
	buffer_load_dwordx4 v[24:27], v184, s[24:27], s42 offen
	s_waitcnt vmcnt(12)
	v_cvt_pk_bf16_f32 v23, v22, v23
	v_cvt_pk_bf16_f32 v22, v20, v21
	s_waitcnt lgkmcnt(5)
	v_mfma_f32_16x16x32_bf16 v[168:171], v[218:221], v[206:209], v[168:171]
	ds_write_b64 v185, v[22:23] offset:34880
	s_waitcnt lgkmcnt(4)
	v_mfma_f32_16x16x32_bf16 v[164:167], v[248:251], v[206:209], v[164:167]
	s_waitcnt lgkmcnt(2)
	v_mfma_f32_16x16x32_bf16 v[160:163], v[252:255], v[206:209], v[160:163]
	v_mfma_f32_16x16x32_bf16 v[156:159], v[244:247], v[210:213], v[156:159]
	ds_read_b128 v[206:209], v186 offset:7168
	v_mfma_f32_16x16x32_bf16 v[152:155], v[218:221], v[210:213], v[152:155]
	v_mfma_f32_16x16x32_bf16 v[148:151], v[248:251], v[210:213], v[148:151]
	v_mfma_f32_16x16x32_bf16 v[144:147], v[252:255], v[210:213], v[144:147]
	s_waitcnt lgkmcnt(2)
	v_mfma_f32_16x16x32_bf16 v[132:135], v[244:247], v[202:205], v[132:135]
	ds_read_b128 v[210:213], v186 offset:9216
	buffer_load_dwordx4 v[20:23], v184, s[28:31], s37 offen
	s_waitcnt vmcnt(12)
	v_cvt_pk_bf16_f32 v7, v6, v7
	v_cvt_pk_bf16_f32 v6, v4, v5
	v_mfma_f32_16x16x32_bf16 v[124:127], v[218:221], v[202:205], v[124:127]
	ds_write_b64 v185, v[6:7] offset:43584
	v_mfma_f32_16x16x32_bf16 v[120:123], v[248:251], v[202:205], v[120:123]
	v_mfma_f32_16x16x32_bf16 v[140:143], v[252:255], v[202:205], v[140:143]
	s_waitcnt lgkmcnt(2)
	v_mfma_f32_16x16x32_bf16 v[136:139], v[244:247], v[206:209], v[136:139]
	ds_read_b128 v[202:205], v186 offset:11264
	v_mfma_f32_16x16x32_bf16 v[128:131], v[218:221], v[206:209], v[128:131]
	v_mfma_f32_16x16x32_bf16 v[116:119], v[248:251], v[206:209], v[116:119]
	v_mfma_f32_16x16x32_bf16 v[112:115], v[252:255], v[206:209], v[112:115]
	s_waitcnt lgkmcnt(2)
	v_mfma_f32_16x16x32_bf16 v[100:103], v[244:247], v[210:213], v[100:103]
	ds_read_b128 v[206:209], v186 offset:13312
	buffer_load_dwordx4 v[4:7], v184, s[28:31], s38 offen
	s_waitcnt vmcnt(12)
	v_cvt_pk_bf16_f32 v11, v10, v11
	v_cvt_pk_bf16_f32 v10, v8, v9
	v_mfma_f32_16x16x32_bf16 v[92:95], v[218:221], v[210:213], v[92:95]
	ds_write_b64 v185, v[10:11] offset:52288
	v_mfma_f32_16x16x32_bf16 v[88:91], v[248:251], v[210:213], v[88:91]
	v_mfma_f32_16x16x32_bf16 v[108:111], v[252:255], v[210:213], v[108:111]
	s_waitcnt lgkmcnt(2)
	v_mfma_f32_16x16x32_bf16 v[104:107], v[244:247], v[202:205], v[104:107]
	ds_read_b128 v[210:213], v186 offset:15360
	v_mfma_f32_16x16x32_bf16 v[96:99], v[218:221], v[202:205], v[96:99]
	v_mfma_f32_16x16x32_bf16 v[84:87], v[248:251], v[202:205], v[84:87]
	v_mfma_f32_16x16x32_bf16 v[80:83], v[252:255], v[202:205], v[80:83]
	s_waitcnt lgkmcnt(2)
	v_mfma_f32_16x16x32_bf16 v[72:75], v[244:247], v[206:209], v[72:75]
	ds_read_b128 v[238:241], v186 offset:17408
	buffer_load_dwordx4 v[8:11], v184, s[28:31], s39 offen
	s_waitcnt vmcnt(12)
	v_cvt_pk_bf16_f32 v19, v18, v19
	v_cvt_pk_bf16_f32 v18, v16, v17
	v_mfma_f32_16x16x32_bf16 v[64:67], v[218:221], v[206:209], v[64:67]
	ds_write_b64 v185, v[18:19] offset:60992
	v_mfma_f32_16x16x32_bf16 v[60:63], v[248:251], v[206:209], v[60:63]
	v_mfma_f32_16x16x32_bf16 v[76:79], v[252:255], v[206:209], v[76:79]
	s_waitcnt lgkmcnt(2)
	v_mfma_f32_16x16x32_bf16 v[68:71], v[244:247], v[210:213], v[68:71]
	buffer_load_dwordx4 v[16:19], v184, s[28:31], s42 offen
	v_mfma_f32_16x16x32_bf16 v[56:59], v[218:221], v[210:213], v[56:59]
	v_mfma_f32_16x16x32_bf16 v[52:55], v[248:251], v[210:213], v[52:55]
	v_mfma_f32_16x16x32_bf16 v[48:51], v[252:255], v[210:213], v[48:51]
	s_waitcnt lgkmcnt(1)
	s_waitcnt vmcnt(8)
	s_mov_b32 m0, s46
	s_waitcnt lgkmcnt(0)
	s_barrier
	ds_read_b64_tr_b16 v[178:179], v188 offset:34816
	ds_read_b64_tr_b16 v[176:177], v187 offset:34816
	ds_read_b64_tr_b16 v[180:181], v187 offset:34848
	ds_read_b64_tr_b16 v[198:199], v187 offset:34880
	ds_read_b64_tr_b16 v[202:203], v187 offset:34912
	ds_read_b128 v[206:209], v186 offset:36864
	ds_read_b64_tr_b16 v[182:183], v188 offset:34848
	ds_read_b64_tr_b16 v[200:201], v188 offset:34880
	ds_read_b64_tr_b16 v[204:205], v188 offset:34912
	ds_read_b128 v[210:213], v186 offset:38912
	ds_read_b128 v[214:217], v186 offset:40960
	buffer_load_dwordx4 v189, s[20:23], s36 offen lds
	s_mov_b32 m0, s86
	v_mfma_f32_16x16x32_bf16 v[44:47], v[244:247], v[238:241], v[44:47]
	v_mfma_f32_16x16x32_bf16 v[40:43], v[218:221], v[238:241], v[40:43]
	v_mfma_f32_16x16x32_bf16 v[36:39], v[248:251], v[238:241], v[36:39]
	v_mfma_f32_16x16x32_bf16 v[32:35], v[252:255], v[238:241], v[32:35]
	s_waitcnt lgkmcnt(5)
	v_mfma_f32_16x16x32_bf16 v[172:175], v[176:179], v[206:209], v[172:175]
	buffer_load_dwordx4 v192, s[20:23], s36 offen lds
	s_add_i32 s37, s17, 0xfffa0000
	s_waitcnt lgkmcnt(4)
	v_mfma_f32_16x16x32_bf16 v[168:171], v[180:183], v[206:209], v[168:171]
	s_waitcnt lgkmcnt(3)
	v_mfma_f32_16x16x32_bf16 v[164:167], v[198:201], v[206:209], v[164:167]
	s_waitcnt lgkmcnt(2)
	v_mfma_f32_16x16x32_bf16 v[160:163], v[202:205], v[206:209], v[160:163]
	s_waitcnt lgkmcnt(1)
	v_mfma_f32_16x16x32_bf16 v[156:159], v[176:179], v[210:213], v[156:159]
	s_mov_b32 m0, s89
	s_nop 0
	buffer_load_dwordx4 v191, s[20:23], s36 offen lds
	ds_read_b128 v[206:209], v186 offset:43008
	s_waitcnt vmcnt(10)
	v_cvt_pk_bf16_f32 v15, v14, v15
	v_cvt_pk_bf16_f32 v14, v12, v13
	v_mfma_f32_16x16x32_bf16 v[152:155], v[180:183], v[210:213], v[152:155]
	ds_write_b64 v185, v[14:15]
	v_mfma_f32_16x16x32_bf16 v[148:151], v[198:201], v[210:213], v[148:151]
	s_mov_b32 m0, s90
	s_nop 0
	buffer_load_dwordx4 v190, s[20:23], s36 offen lds
	v_mfma_f32_16x16x32_bf16 v[144:147], v[202:205], v[210:213], v[144:147]
	s_waitcnt lgkmcnt(2)
	v_mfma_f32_16x16x32_bf16 v[132:135], v[176:179], v[214:217], v[132:135]
	s_mov_b32 m0, s91
	s_nop 0
	buffer_load_dwordx4 v193, s[20:23], s36 offen lds
	ds_read_b128 v[210:213], v186 offset:45056
	v_mfma_f32_16x16x32_bf16 v[124:127], v[180:183], v[214:217], v[124:127]
	v_mfma_f32_16x16x32_bf16 v[120:123], v[198:201], v[214:217], v[120:123]
	v_mfma_f32_16x16x32_bf16 v[140:143], v[202:205], v[214:217], v[140:143]
	s_waitcnt lgkmcnt(2)
	v_mfma_f32_16x16x32_bf16 v[136:139], v[176:179], v[206:209], v[136:139]
	ds_read_b128 v[214:217], v186 offset:47104
	buffer_load_dwordx4 v[12:15], v184, s[24:27], s37 offen
	s_waitcnt vmcnt(12)
	v_cvt_pk_bf16_f32 v3, v2, v3
	v_cvt_pk_bf16_f32 v2, v0, v1
	v_mfma_f32_16x16x32_bf16 v[128:131], v[180:183], v[206:209], v[128:131]
	ds_write_b64 v185, v[2:3] offset:8704
	v_mfma_f32_16x16x32_bf16 v[116:119], v[198:201], v[206:209], v[116:119]
	v_mfma_f32_16x16x32_bf16 v[112:115], v[202:205], v[206:209], v[112:115]
	s_add_i32 s38, s17, 0xfffc0000
	s_waitcnt lgkmcnt(2)
	v_mfma_f32_16x16x32_bf16 v[100:103], v[176:179], v[210:213], v[100:103]
	ds_read_b128 v[206:209], v186 offset:49152
	v_mfma_f32_16x16x32_bf16 v[92:95], v[180:183], v[210:213], v[92:95]
	v_mfma_f32_16x16x32_bf16 v[88:91], v[198:201], v[210:213], v[88:91]
	v_mfma_f32_16x16x32_bf16 v[108:111], v[202:205], v[210:213], v[108:111]
	s_waitcnt lgkmcnt(2)
	v_mfma_f32_16x16x32_bf16 v[104:107], v[176:179], v[214:217], v[104:107]
	ds_read_b128 v[210:213], v186 offset:51200
	buffer_load_dwordx4 v[0:3], v184, s[24:27], s38 offen
	s_waitcnt vmcnt(12)
	v_cvt_pk_bf16_f32 v31, v30, v31
	v_cvt_pk_bf16_f32 v30, v28, v29
	v_mfma_f32_16x16x32_bf16 v[96:99], v[180:183], v[214:217], v[96:99]
	ds_write_b64 v185, v[30:31] offset:17408
	v_mfma_f32_16x16x32_bf16 v[84:87], v[198:201], v[214:217], v[84:87]
	v_mfma_f32_16x16x32_bf16 v[80:83], v[202:205], v[214:217], v[80:83]
	s_add_i32 s39, s17, 0xfffe0000
	s_waitcnt lgkmcnt(2)
	v_mfma_f32_16x16x32_bf16 v[72:75], v[176:179], v[206:209], v[72:75]
	ds_read_b128 v[214:217], v186 offset:53248
	v_mfma_f32_16x16x32_bf16 v[64:67], v[180:183], v[206:209], v[64:67]
	v_mfma_f32_16x16x32_bf16 v[60:63], v[198:201], v[206:209], v[60:63]
	v_mfma_f32_16x16x32_bf16 v[76:79], v[202:205], v[206:209], v[76:79]
	s_waitcnt lgkmcnt(2)
	v_mfma_f32_16x16x32_bf16 v[68:71], v[176:179], v[210:213], v[68:71]
	ds_read_b128 v[206:209], v186 offset:37888
	buffer_load_dwordx4 v[28:31], v184, s[24:27], s39 offen
	s_waitcnt vmcnt(12)
	v_cvt_pk_bf16_f32 v27, v26, v27
	v_cvt_pk_bf16_f32 v26, v24, v25
	v_mfma_f32_16x16x32_bf16 v[56:59], v[180:183], v[210:213], v[56:59]
	ds_write_b64 v185, v[26:27] offset:26112
	v_mfma_f32_16x16x32_bf16 v[52:55], v[198:201], v[210:213], v[52:55]
	v_mfma_f32_16x16x32_bf16 v[48:51], v[202:205], v[210:213], v[48:51]
	ds_read_b128 v[210:213], v186 offset:39936
	s_waitcnt lgkmcnt(3)
	v_mfma_f32_16x16x32_bf16 v[44:47], v[176:179], v[214:217], v[44:47]
	ds_read_b64_tr_b16 v[246:247], v188 offset:52224
	ds_read_b64_tr_b16 v[220:221], v188 offset:52256
	ds_read_b64_tr_b16 v[244:245], v187 offset:52224
	ds_read_b64_tr_b16 v[218:219], v187 offset:52256
	v_mfma_f32_16x16x32_bf16 v[40:43], v[180:183], v[214:217], v[40:43]
	ds_read_b64_tr_b16 v[248:249], v187 offset:52288
	ds_read_b64_tr_b16 v[250:251], v188 offset:52288
	v_mfma_f32_16x16x32_bf16 v[36:39], v[198:201], v[214:217], v[36:39]
	ds_read_b64_tr_b16 v[252:253], v187 offset:52320
	ds_read_b64_tr_b16 v[254:255], v188 offset:52320
	v_mfma_f32_16x16x32_bf16 v[32:35], v[202:205], v[214:217], v[32:35]
	s_waitcnt lgkmcnt(5)
	v_mfma_f32_16x16x32_bf16 v[172:175], v[244:247], v[206:209], v[172:175]
	ds_read_b128 v[202:205], v186 offset:41984
	buffer_load_dwordx4 v[24:27], v184, s[24:27], s17 offen
	s_waitcnt vmcnt(12)
; #define G_ENDTILE(VM) do { asm volatile("s_waitcnt vmcnt(" #VM ")" ::: "memory"); \
;         asm volatile("s_waitcnt lgkmcnt(0)" ::: "memory"); __builtin_amdgcn_s_barrier(); asm volatile("" ::: "memory"); } while (0)
;     ...
;         for (int t = 0; t < nt - 2; t += 2) {
;             G_TILE(G_A0, G_B0, true, G_B1, G_A1, t + 1, true, t + 2, (void)0);
;             G_ENDTILE(8);
;             G_TILE(G_A1, G_B1, true, G_B0, G_A0, t + 2, true, t + 3, (void)0);
;             G_ENDTILE(8);
;         }
	v_cvt_pk_bf16_f32 v23, v22, v23
	v_cvt_pk_bf16_f32 v22, v20, v21
	s_waitcnt lgkmcnt(5)
	v_mfma_f32_16x16x32_bf16 v[168:171], v[218:221], v[206:209], v[168:171]
	ds_write_b64 v185, v[22:23] offset:64
	s_waitcnt lgkmcnt(4)
	v_mfma_f32_16x16x32_bf16 v[164:167], v[248:251], v[206:209], v[164:167]
	s_waitcnt lgkmcnt(2)
	v_mfma_f32_16x16x32_bf16 v[160:163], v[252:255], v[206:209], v[160:163]
	v_mfma_f32_16x16x32_bf16 v[156:159], v[244:247], v[210:213], v[156:159]
	ds_read_b128 v[206:209], v186 offset:44032
	v_mfma_f32_16x16x32_bf16 v[152:155], v[218:221], v[210:213], v[152:155]
	v_mfma_f32_16x16x32_bf16 v[148:151], v[248:251], v[210:213], v[148:151]
	v_mfma_f32_16x16x32_bf16 v[144:147], v[252:255], v[210:213], v[144:147]
	s_waitcnt lgkmcnt(2)
	v_mfma_f32_16x16x32_bf16 v[132:135], v[244:247], v[202:205], v[132:135]
	ds_read_b128 v[210:213], v186 offset:46080
	buffer_load_dwordx4 v[20:23], v184, s[28:31], s37 offen
	s_waitcnt vmcnt(12)
	v_cvt_pk_bf16_f32 v7, v6, v7
	v_cvt_pk_bf16_f32 v6, v4, v5
	v_mfma_f32_16x16x32_bf16 v[124:127], v[218:221], v[202:205], v[124:127]
	ds_write_b64 v185, v[6:7] offset:8768
	v_mfma_f32_16x16x32_bf16 v[120:123], v[248:251], v[202:205], v[120:123]
	v_mfma_f32_16x16x32_bf16 v[140:143], v[252:255], v[202:205], v[140:143]
	s_waitcnt lgkmcnt(2)
	v_mfma_f32_16x16x32_bf16 v[136:139], v[244:247], v[206:209], v[136:139]
	ds_read_b128 v[202:205], v186 offset:48128
	v_mfma_f32_16x16x32_bf16 v[128:131], v[218:221], v[206:209], v[128:131]
	v_mfma_f32_16x16x32_bf16 v[116:119], v[248:251], v[206:209], v[116:119]
	v_mfma_f32_16x16x32_bf16 v[112:115], v[252:255], v[206:209], v[112:115]
	s_waitcnt lgkmcnt(2)
	v_mfma_f32_16x16x32_bf16 v[100:103], v[244:247], v[210:213], v[100:103]
	ds_read_b128 v[206:209], v186 offset:50176
	buffer_load_dwordx4 v[4:7], v184, s[28:31], s38 offen
	s_waitcnt vmcnt(12)
	v_cvt_pk_bf16_f32 v11, v10, v11
	v_cvt_pk_bf16_f32 v10, v8, v9
	v_mfma_f32_16x16x32_bf16 v[92:95], v[218:221], v[210:213], v[92:95]
	ds_write_b64 v185, v[10:11] offset:17472
	v_mfma_f32_16x16x32_bf16 v[88:91], v[248:251], v[210:213], v[88:91]
	v_mfma_f32_16x16x32_bf16 v[108:111], v[252:255], v[210:213], v[108:111]
	s_waitcnt lgkmcnt(2)
	v_mfma_f32_16x16x32_bf16 v[104:107], v[244:247], v[202:205], v[104:107]
	ds_read_b128 v[210:213], v186 offset:52224
	v_mfma_f32_16x16x32_bf16 v[96:99], v[218:221], v[202:205], v[96:99]
	v_mfma_f32_16x16x32_bf16 v[84:87], v[248:251], v[202:205], v[84:87]
	v_mfma_f32_16x16x32_bf16 v[80:83], v[252:255], v[202:205], v[80:83]
	s_waitcnt lgkmcnt(2)
	v_mfma_f32_16x16x32_bf16 v[72:75], v[244:247], v[206:209], v[72:75]
	ds_read_b128 v[238:241], v186 offset:54272
	buffer_load_dwordx4 v[8:11], v184, s[28:31], s39 offen
	s_waitcnt vmcnt(12)
	v_cvt_pk_bf16_f32 v19, v18, v19
	v_cvt_pk_bf16_f32 v18, v16, v17
	v_mfma_f32_16x16x32_bf16 v[64:67], v[218:221], v[206:209], v[64:67]
	ds_write_b64 v185, v[18:19] offset:26176
	v_mfma_f32_16x16x32_bf16 v[60:63], v[248:251], v[206:209], v[60:63]
	v_mfma_f32_16x16x32_bf16 v[76:79], v[252:255], v[206:209], v[76:79]
	s_waitcnt lgkmcnt(2)
	v_mfma_f32_16x16x32_bf16 v[68:71], v[244:247], v[210:213], v[68:71]
	buffer_load_dwordx4 v[16:19], v184, s[28:31], s17 offen
	v_mfma_f32_16x16x32_bf16 v[56:59], v[218:221], v[210:213], v[56:59]
	v_mfma_f32_16x16x32_bf16 v[52:55], v[248:251], v[210:213], v[52:55]
	v_mfma_f32_16x16x32_bf16 v[48:51], v[252:255], v[210:213], v[48:51]
	s_waitcnt lgkmcnt(1)
	s_waitcnt vmcnt(8)
	s_waitcnt lgkmcnt(0)
	s_barrier
	s_add_i32 s16, s16, 2
	s_add_i32 s17, s17, 0x100000
	s_addk_i32 s36, 0x100
	s_cmp_ge_i32 s16, s97
	s_cbranch_scc0 .LBB0_651

; #define LAS __attribute__((address_space(3)))
;     ...
;         U nxt = cur;
;         const bool has_next = sched.get(ui + 1, nxt);
; DI bool moe_find(const Ctx& c, int qi, int NT, int& e, int& nt, int& mt, int& cn, int& hb) {
;     LAS int* S = (LAS int*)(c.lds + MS_OFF);
;     const int nown = __builtin_amdgcn_readfirstlane(S[0]); int accu = 0;
;     for (int k = 0; k < nown; ++k) { const int mc = __builtin_amdgcn_readfirstlane(S[9 + 4 * k]);
;         if (qi < accu + NT * mc) { const int loc = qi - accu; nt = loc / mc; mt = loc - nt * mc;
;             e = __builtin_amdgcn_readfirstlane(S[8 + 4 * k]); cn = __builtin_amdgcn_readfirstlane(S[10 + 4 * k]); hb = __builtin_amdgcn_readfirstlane(S[11 + 4 * k]); return true; }
;         accu += NT * mc; }
.LBB0_653:
	v_mov_b32_e32 v176, s5
	ds_read_b32 v176, v176
	s_add_i32 s92, s92, 1
	s_waitcnt lgkmcnt(0)
	v_readfirstlane_b32 s16, v176
	s_cmp_lt_i32 s16, 1
	s_cbranch_scc1 .LBB0_660
	s_mul_i32 s25, s92, s70
	s_add_i32 s16, s16, -1
	s_add_i32 s100, s33, s92
	s_and_b32 s100, s100, 31
	s_cmp_eq_u32 s70, 32
	s_cselect_b32 s100, s100, s33
	s_add_i32 s25, s25, s100
	s_mov_b32 s27, s101
	s_sub_i32 s100, s98, s52
	s_lshr_b32 s100, s100, 4
	s_sub_i32 s16, s16, s100
	v_mov_b32_e32 v176, s16
	s_mov_b32 s26, s98

; DI bool moe_find(const Ctx& c, int qi, int NT, int& e, int& nt, int& mt, int& cn, int& hb) {
;     ...
;         if (qi < accu + NT * mc) { const int loc = qi - accu; nt = loc / mc; mt = loc - nt * mc;
;             e = __builtin_amdgcn_readfirstlane(S[8 + 4 * k]); cn = __builtin_amdgcn_readfirstlane(S[10 + 4 * k]); hb = __builtin_amdgcn_readfirstlane(S[11 + 4 * k]); return true; }
.LBB0_659:
	s_add_i32 s98, s26, -16
	s_mov_b32 s101, s27
	s_lshl_b32 s27, s30, 10
	s_mul_i32 s26, s31, 0x120
	s_branch .LBB0_661

; #define G_ENDTILE(VM) do { asm volatile("s_waitcnt vmcnt(" #VM ")" ::: "memory"); \
;         asm volatile("s_waitcnt lgkmcnt(0)" ::: "memory"); __builtin_amdgcn_s_barrier(); asm volatile("" ::: "memory"); } while (0)
;     ...
;     for (int ui = 0;; ++ui) {
; #pragma unroll
;         for (int m = 0; m < MF; ++m)
; #pragma unroll
;             for (int n = 0; n < 4; ++n) acc[m][n] = (f32x4){0.f, 0.f, 0.f, 0.f};
;         for (int t = 0; t < nt - 2; t += 2) {
;             G_TILE(G_A0, G_B0, true, G_B1, G_A1, t + 1, true, t + 2, (void)0);
;             G_ENDTILE(8);
;             G_TILE(G_A1, G_B1, true, G_B0, G_A0, t + 2, true, t + 3, (void)0);
.LBB0_861:
	s_andn2_b64 vcc, exec, s[28:29]
	v_mov_b32_e32 v175, 0
	s_cbranch_vccnz .LBB0_864
	s_mov_b32 s8, 0
	s_mov_b32 s9, 0x1e0000
	s_movk_i32 s36, 0x100
	s_waitcnt vmcnt(1)
	s_waitcnt vmcnt(0)
	s_cmp_lt_u32 s99, 9
	s_cbranch_scc1 .Lslow_P6
	s_mov_b32 m0, s85
	s_add_i32 s38, s36, 0xffffff80
	ds_read_b64_tr_b16 v[178:179], v206
	ds_read_b64_tr_b16 v[176:177], v205
	ds_read_b64_tr_b16 v[180:181], v205 offset:32
	ds_read_b64_tr_b16 v[184:185], v205 offset:64
	ds_read_b64_tr_b16 v[188:189], v205 offset:96
	ds_read_b128 v[192:195], v199
	ds_read_b64_tr_b16 v[182:183], v206 offset:32
	ds_read_b64_tr_b16 v[186:187], v206 offset:64
	ds_read_b64_tr_b16 v[190:191], v206 offset:96
	ds_read_b128 v[208:211], v199 offset:2048
	ds_read_b128 v[212:215], v199 offset:4096
	buffer_load_dwordx4 v200, s[20:23], s38 offen lds
	s_mov_b32 m0, s86
	s_waitcnt lgkmcnt(0)
	v_mfma_f32_16x16x32_bf16 v[172:175], v[176:179], v[192:195], 0
	buffer_load_dwordx4 v201, s[20:23], s38 offen lds
	v_mfma_f32_16x16x32_bf16 v[168:171], v[180:183], v[192:195], 0
	v_mfma_f32_16x16x32_bf16 v[164:167], v[184:187], v[192:195], 0
	v_mfma_f32_16x16x32_bf16 v[160:163], v[188:191], v[192:195], 0
	v_mfma_f32_16x16x32_bf16 v[156:159], v[176:179], v[208:211], 0
	s_mov_b32 m0, s87
	s_nop 0
	buffer_load_dwordx4 v202, s[20:23], s38 offen lds
	ds_read_b128 v[192:195], v199 offset:6144
	s_waitcnt vmcnt(10)
	v_cvt_pk_bf16_f32 v23, v22, v23
	v_cvt_pk_bf16_f32 v22, v20, v21
	v_mfma_f32_16x16x32_bf16 v[152:155], v[180:183], v[208:211], 0
	ds_write_b64 v198, v[22:23] offset:34816
	v_mfma_f32_16x16x32_bf16 v[148:151], v[184:187], v[208:211], 0
	s_mov_b32 m0, s88
	s_nop 0
	buffer_load_dwordx4 v203, s[20:23], s38 offen lds
	v_mfma_f32_16x16x32_bf16 v[144:147], v[188:191], v[208:211], 0
	v_mfma_f32_16x16x32_bf16 v[132:135], v[176:179], v[212:215], 0
	s_mov_b32 m0, s89
	s_nop 0
	buffer_load_dwordx4 v204, s[20:23], s38 offen lds
	s_add_i32 s38, s9, 0xfff20000
	ds_read_b128 v[208:211], v199 offset:8192
	v_mfma_f32_16x16x32_bf16 v[124:127], v[180:183], v[212:215], 0
	v_mfma_f32_16x16x32_bf16 v[120:123], v[184:187], v[212:215], 0
	v_mfma_f32_16x16x32_bf16 v[140:143], v[188:191], v[212:215], 0
	s_waitcnt lgkmcnt(2)
	v_mfma_f32_16x16x32_bf16 v[136:139], v[176:179], v[192:195], 0
	ds_read_b128 v[212:215], v199 offset:10240
	buffer_load_dwordx4 v[20:23], v197, s[24:27], s38 offen
	s_waitcnt vmcnt(11)
	v_cvt_pk_bf16_f32 v31, v30, v31
	v_cvt_pk_bf16_f32 v30, v28, v29
	v_mfma_f32_16x16x32_bf16 v[128:131], v[180:183], v[192:195], 0
	ds_write_b64 v198, v[30:31] offset:43520
	v_mfma_f32_16x16x32_bf16 v[116:119], v[184:187], v[192:195], 0
	v_mfma_f32_16x16x32_bf16 v[112:115], v[188:191], v[192:195], 0
	s_add_i32 s39, s9, 0xfff40000
	s_waitcnt lgkmcnt(2)
	v_mfma_f32_16x16x32_bf16 v[100:103], v[176:179], v[208:211], 0
	ds_read_b128 v[192:195], v199 offset:12288
	v_mfma_f32_16x16x32_bf16 v[92:95], v[180:183], v[208:211], 0
	v_mfma_f32_16x16x32_bf16 v[88:91], v[184:187], v[208:211], 0
	v_mfma_f32_16x16x32_bf16 v[108:111], v[188:191], v[208:211], 0
	s_waitcnt lgkmcnt(2)
	v_mfma_f32_16x16x32_bf16 v[104:107], v[176:179], v[212:215], 0
	ds_read_b128 v[208:211], v199 offset:14336
	v_cvt_pk_bf16_f32 v19, v18, v19
	v_cvt_pk_bf16_f32 v18, v16, v17
	v_mfma_f32_16x16x32_bf16 v[96:99], v[180:183], v[212:215], 0
	ds_write_b64 v198, v[18:19] offset:52224
	v_mfma_f32_16x16x32_bf16 v[84:87], v[184:187], v[212:215], 0
	v_mfma_f32_16x16x32_bf16 v[80:83], v[188:191], v[212:215], 0
	s_add_i32 s43, s9, 0xfff60000
	buffer_load_dwordx4 v[28:31], v197, s[24:27], s39 offen
	s_waitcnt lgkmcnt(2)
	v_mfma_f32_16x16x32_bf16 v[72:75], v[176:179], v[192:195], 0
	ds_read_b128 v[212:215], v199 offset:16384
	v_mfma_f32_16x16x32_bf16 v[64:67], v[180:183], v[192:195], 0
	v_mfma_f32_16x16x32_bf16 v[60:63], v[184:187], v[192:195], 0
	v_mfma_f32_16x16x32_bf16 v[76:79], v[188:191], v[192:195], 0
	s_waitcnt lgkmcnt(2)
	v_mfma_f32_16x16x32_bf16 v[68:71], v[176:179], v[208:211], 0
	ds_read_b128 v[192:195], v199 offset:1024
	buffer_load_dwordx4 v[16:19], v197, s[24:27], s43 offen
	s_waitcnt vmcnt(12)
	v_cvt_pk_bf16_f32 v27, v26, v27
	v_cvt_pk_bf16_f32 v26, v24, v25
	v_mfma_f32_16x16x32_bf16 v[56:59], v[180:183], v[208:211], 0
	ds_write_b64 v198, v[26:27] offset:60928
	v_mfma_f32_16x16x32_bf16 v[52:55], v[184:187], v[208:211], 0
	v_mfma_f32_16x16x32_bf16 v[48:51], v[188:191], v[208:211], 0
	s_add_i32 s45, s9, 0xfff80000
	ds_read_b128 v[208:211], v199 offset:3072
	s_waitcnt lgkmcnt(3)
	v_mfma_f32_16x16x32_bf16 v[44:47], v[176:179], v[212:215], 0
	ds_read_b64_tr_b16 v[246:247], v206 offset:17408
	ds_read_b64_tr_b16 v[218:219], v206 offset:17440
	ds_read_b64_tr_b16 v[244:245], v205 offset:17408
	ds_read_b64_tr_b16 v[216:217], v205 offset:17440
	v_mfma_f32_16x16x32_bf16 v[40:43], v[180:183], v[212:215], 0
	ds_read_b64_tr_b16 v[248:249], v205 offset:17472
	ds_read_b64_tr_b16 v[250:251], v206 offset:17472
	v_mfma_f32_16x16x32_bf16 v[36:39], v[184:187], v[212:215], 0
	ds_read_b64_tr_b16 v[252:253], v205 offset:17504
	ds_read_b64_tr_b16 v[254:255], v206 offset:17504
	v_mfma_f32_16x16x32_bf16 v[32:35], v[188:191], v[212:215], 0
	s_waitcnt lgkmcnt(5)
	v_mfma_f32_16x16x32_bf16 v[172:175], v[244:247], v[192:195], v[172:175]
	ds_read_b128 v[188:191], v199 offset:5120
	buffer_load_dwordx4 v[24:27], v197, s[24:27], s45 offen
	s_waitcnt vmcnt(12)
	v_cvt_pk_bf16_f32 v15, v14, v15
	v_cvt_pk_bf16_f32 v14, v12, v13
	s_waitcnt lgkmcnt(5)
	v_mfma_f32_16x16x32_bf16 v[168:171], v[216:219], v[192:195], v[168:171]
	ds_write_b64 v198, v[14:15] offset:35072
	s_waitcnt lgkmcnt(4)
	v_mfma_f32_16x16x32_bf16 v[164:167], v[248:251], v[192:195], v[164:167]
	s_waitcnt lgkmcnt(2)
	v_mfma_f32_16x16x32_bf16 v[160:163], v[252:255], v[192:195], v[160:163]
	v_mfma_f32_16x16x32_bf16 v[156:159], v[244:247], v[208:211], v[156:159]
	ds_read_b128 v[192:195], v199 offset:7168
	v_mfma_f32_16x16x32_bf16 v[152:155], v[216:219], v[208:211], v[152:155]
	v_mfma_f32_16x16x32_bf16 v[148:151], v[248:251], v[208:211], v[148:151]
	v_mfma_f32_16x16x32_bf16 v[144:147], v[252:255], v[208:211], v[144:147]
	s_waitcnt lgkmcnt(2)
	v_mfma_f32_16x16x32_bf16 v[132:135], v[244:247], v[188:191], v[132:135]
	ds_read_b128 v[208:211], v199 offset:9216
	buffer_load_dwordx4 v[12:15], v197, s[16:19], s38 offen
	s_waitcnt vmcnt(11)
	v_cvt_pk_bf16_f32 v7, v6, v7
	v_cvt_pk_bf16_f32 v6, v4, v5
	v_mfma_f32_16x16x32_bf16 v[124:127], v[216:219], v[188:191], v[124:127]
	ds_write_b64 v198, v[6:7] offset:43776
	v_mfma_f32_16x16x32_bf16 v[120:123], v[248:251], v[188:191], v[120:123]
	v_mfma_f32_16x16x32_bf16 v[140:143], v[252:255], v[188:191], v[140:143]
	s_waitcnt lgkmcnt(2)
	v_mfma_f32_16x16x32_bf16 v[136:139], v[244:247], v[192:195], v[136:139]
	ds_read_b128 v[188:191], v199 offset:11264
	v_mfma_f32_16x16x32_bf16 v[128:131], v[216:219], v[192:195], v[128:131]
	v_mfma_f32_16x16x32_bf16 v[116:119], v[248:251], v[192:195], v[116:119]
	v_mfma_f32_16x16x32_bf16 v[112:115], v[252:255], v[192:195], v[112:115]
	s_waitcnt lgkmcnt(2)
	v_mfma_f32_16x16x32_bf16 v[100:103], v[244:247], v[208:211], v[100:103]
	ds_read_b128 v[192:195], v199 offset:13312
	v_cvt_pk_bf16_f32 v3, v2, v3
	v_cvt_pk_bf16_f32 v2, v0, v1
	v_mfma_f32_16x16x32_bf16 v[92:95], v[216:219], v[208:211], v[92:95]
	ds_write_b64 v198, v[2:3] offset:52480
	v_mfma_f32_16x16x32_bf16 v[88:91], v[248:251], v[208:211], v[88:91]
	v_mfma_f32_16x16x32_bf16 v[108:111], v[252:255], v[208:211], v[108:111]
	buffer_load_dwordx4 v[4:7], v197, s[16:19], s39 offen
	s_waitcnt lgkmcnt(2)
	v_mfma_f32_16x16x32_bf16 v[104:107], v[244:247], v[188:191], v[104:107]
	ds_read_b128 v[208:211], v199 offset:15360
	v_mfma_f32_16x16x32_bf16 v[96:99], v[216:219], v[188:191], v[96:99]
	v_mfma_f32_16x16x32_bf16 v[84:87], v[248:251], v[188:191], v[84:87]
	v_mfma_f32_16x16x32_bf16 v[80:83], v[252:255], v[188:191], v[80:83]
	s_waitcnt lgkmcnt(2)
	v_mfma_f32_16x16x32_bf16 v[72:75], v[244:247], v[192:195], v[72:75]
	ds_read_b128 v[236:239], v199 offset:17408
	buffer_load_dwordx4 v[0:3], v197, s[16:19], s43 offen
	s_waitcnt vmcnt(12)
	v_cvt_pk_bf16_f32 v11, v10, v11
	v_cvt_pk_bf16_f32 v10, v8, v9
	v_mfma_f32_16x16x32_bf16 v[64:67], v[216:219], v[192:195], v[64:67]
	ds_write_b64 v198, v[10:11] offset:61184
	v_mfma_f32_16x16x32_bf16 v[60:63], v[248:251], v[192:195], v[60:63]
	v_mfma_f32_16x16x32_bf16 v[76:79], v[252:255], v[192:195], v[76:79]
	s_waitcnt lgkmcnt(2)
	v_mfma_f32_16x16x32_bf16 v[68:71], v[244:247], v[208:211], v[68:71]
	buffer_load_dwordx4 v[8:11], v197, s[16:19], s45 offen
	v_mfma_f32_16x16x32_bf16 v[56:59], v[216:219], v[208:211], v[56:59]
	v_mfma_f32_16x16x32_bf16 v[52:55], v[248:251], v[208:211], v[52:55]
	v_mfma_f32_16x16x32_bf16 v[48:51], v[252:255], v[208:211], v[48:51]
	s_waitcnt lgkmcnt(1)
	s_waitcnt vmcnt(8)
	s_mov_b32 m0, s49
	s_waitcnt lgkmcnt(0)
	s_barrier
	ds_read_b64_tr_b16 v[178:179], v206 offset:34816
	ds_read_b64_tr_b16 v[176:177], v205 offset:34816
	ds_read_b64_tr_b16 v[180:181], v205 offset:34848
	ds_read_b64_tr_b16 v[184:185], v205 offset:34880
	ds_read_b64_tr_b16 v[188:189], v205 offset:34912
	ds_read_b128 v[192:195], v199 offset:36864
	ds_read_b64_tr_b16 v[182:183], v206 offset:34848
	ds_read_b64_tr_b16 v[186:187], v206 offset:34880
	ds_read_b64_tr_b16 v[190:191], v206 offset:34912
	ds_read_b128 v[208:211], v199 offset:38912
	ds_read_b128 v[212:215], v199 offset:40960
	buffer_load_dwordx4 v200, s[20:23], s36 offen lds
	s_mov_b32 m0, s68
	v_mfma_f32_16x16x32_bf16 v[44:47], v[244:247], v[236:239], v[44:47]
	v_mfma_f32_16x16x32_bf16 v[40:43], v[216:219], v[236:239], v[40:43]
	v_mfma_f32_16x16x32_bf16 v[36:39], v[248:251], v[236:239], v[36:39]
	v_mfma_f32_16x16x32_bf16 v[32:35], v[252:255], v[236:239], v[32:35]
	s_waitcnt lgkmcnt(5)
	v_mfma_f32_16x16x32_bf16 v[172:175], v[176:179], v[192:195], v[172:175]
	buffer_load_dwordx4 v201, s[20:23], s36 offen lds
	s_add_i32 s38, s9, 0xfffa0000
	s_waitcnt lgkmcnt(4)
	v_mfma_f32_16x16x32_bf16 v[168:171], v[180:183], v[192:195], v[168:171]
	s_waitcnt lgkmcnt(3)
	v_mfma_f32_16x16x32_bf16 v[164:167], v[184:187], v[192:195], v[164:167]
	s_waitcnt lgkmcnt(2)
	v_mfma_f32_16x16x32_bf16 v[160:163], v[188:191], v[192:195], v[160:163]
	s_waitcnt lgkmcnt(1)
	v_mfma_f32_16x16x32_bf16 v[156:159], v[176:179], v[208:211], v[156:159]
	s_mov_b32 m0, s77
	s_nop 0
	buffer_load_dwordx4 v202, s[20:23], s36 offen lds
	ds_read_b128 v[192:195], v199 offset:43008
	s_waitcnt vmcnt(10)
	v_cvt_pk_bf16_f32 v23, v22, v23
	v_cvt_pk_bf16_f32 v22, v20, v21
	v_mfma_f32_16x16x32_bf16 v[152:155], v[180:183], v[208:211], v[152:155]
	ds_write_b64 v198, v[22:23]
	v_mfma_f32_16x16x32_bf16 v[148:151], v[184:187], v[208:211], v[148:151]
	s_mov_b32 m0, s78
	s_nop 0
	buffer_load_dwordx4 v203, s[20:23], s36 offen lds
	v_mfma_f32_16x16x32_bf16 v[144:147], v[188:191], v[208:211], v[144:147]
	s_waitcnt lgkmcnt(2)
	v_mfma_f32_16x16x32_bf16 v[132:135], v[176:179], v[212:215], v[132:135]
	s_mov_b32 m0, s79
	s_nop 0
	buffer_load_dwordx4 v204, s[20:23], s36 offen lds
	ds_read_b128 v[208:211], v199 offset:45056
	v_mfma_f32_16x16x32_bf16 v[124:127], v[180:183], v[212:215], v[124:127]
	v_mfma_f32_16x16x32_bf16 v[120:123], v[184:187], v[212:215], v[120:123]
	v_mfma_f32_16x16x32_bf16 v[140:143], v[188:191], v[212:215], v[140:143]
	s_waitcnt lgkmcnt(2)
; #define G_ENDTILE(VM) do { asm volatile("s_waitcnt vmcnt(" #VM ")" ::: "memory"); \
;         asm volatile("s_waitcnt lgkmcnt(0)" ::: "memory"); __builtin_amdgcn_s_barrier(); asm volatile("" ::: "memory"); } while (0)
;     ...
;         for (int t = 0; t < nt - 2; t += 2) {
;             G_TILE(G_A0, G_B0, true, G_B1, G_A1, t + 1, true, t + 2, (void)0);
;             G_ENDTILE(8);
;             G_TILE(G_A1, G_B1, true, G_B0, G_A0, t + 2, true, t + 3, (void)0);
;             G_ENDTILE(8);
;         }
	v_mfma_f32_16x16x32_bf16 v[136:139], v[176:179], v[192:195], v[136:139]
	ds_read_b128 v[212:215], v199 offset:47104
	buffer_load_dwordx4 v[20:23], v197, s[24:27], s38 offen
	s_waitcnt vmcnt(12)
	v_cvt_pk_bf16_f32 v31, v30, v31
	v_cvt_pk_bf16_f32 v30, v28, v29
	v_mfma_f32_16x16x32_bf16 v[128:131], v[180:183], v[192:195], v[128:131]
	ds_write_b64 v198, v[30:31] offset:8704
	v_mfma_f32_16x16x32_bf16 v[116:119], v[184:187], v[192:195], v[116:119]
	v_mfma_f32_16x16x32_bf16 v[112:115], v[188:191], v[192:195], v[112:115]
	s_add_i32 s39, s9, 0xfffc0000
	s_waitcnt lgkmcnt(2)
	v_mfma_f32_16x16x32_bf16 v[100:103], v[176:179], v[208:211], v[100:103]
	ds_read_b128 v[192:195], v199 offset:49152
	v_mfma_f32_16x16x32_bf16 v[92:95], v[180:183], v[208:211], v[92:95]
	v_mfma_f32_16x16x32_bf16 v[88:91], v[184:187], v[208:211], v[88:91]
	v_mfma_f32_16x16x32_bf16 v[108:111], v[188:191], v[208:211], v[108:111]
	s_waitcnt lgkmcnt(2)
	v_mfma_f32_16x16x32_bf16 v[104:107], v[176:179], v[212:215], v[104:107]
	ds_read_b128 v[208:211], v199 offset:51200
	buffer_load_dwordx4 v[28:31], v197, s[24:27], s39 offen
	s_waitcnt vmcnt(12)
	v_cvt_pk_bf16_f32 v19, v18, v19
	v_cvt_pk_bf16_f32 v18, v16, v17
	v_mfma_f32_16x16x32_bf16 v[96:99], v[180:183], v[212:215], v[96:99]
	ds_write_b64 v198, v[18:19] offset:17408
	v_mfma_f32_16x16x32_bf16 v[84:87], v[184:187], v[212:215], v[84:87]
	v_mfma_f32_16x16x32_bf16 v[80:83], v[188:191], v[212:215], v[80:83]
	s_add_i32 s43, s9, 0xfffe0000
	s_waitcnt lgkmcnt(2)
	v_mfma_f32_16x16x32_bf16 v[72:75], v[176:179], v[192:195], v[72:75]
	ds_read_b128 v[212:215], v199 offset:53248
	v_mfma_f32_16x16x32_bf16 v[64:67], v[180:183], v[192:195], v[64:67]
	v_mfma_f32_16x16x32_bf16 v[60:63], v[184:187], v[192:195], v[60:63]
	v_mfma_f32_16x16x32_bf16 v[76:79], v[188:191], v[192:195], v[76:79]
	s_waitcnt lgkmcnt(2)
	v_mfma_f32_16x16x32_bf16 v[68:71], v[176:179], v[208:211], v[68:71]
	ds_read_b128 v[192:195], v199 offset:37888
	buffer_load_dwordx4 v[16:19], v197, s[24:27], s43 offen
	s_waitcnt vmcnt(12)
	v_cvt_pk_bf16_f32 v27, v26, v27
	v_cvt_pk_bf16_f32 v26, v24, v25
	v_mfma_f32_16x16x32_bf16 v[56:59], v[180:183], v[208:211], v[56:59]
	ds_write_b64 v198, v[26:27] offset:26112
	v_mfma_f32_16x16x32_bf16 v[52:55], v[184:187], v[208:211], v[52:55]
	v_mfma_f32_16x16x32_bf16 v[48:51], v[188:191], v[208:211], v[48:51]
	s_waitcnt lgkmcnt(2)
	v_mfma_f32_16x16x32_bf16 v[44:47], v[176:179], v[212:215], v[44:47]
	ds_read_b128 v[176:179], v199 offset:39936
	v_mfma_f32_16x16x32_bf16 v[40:43], v[180:183], v[212:215], v[40:43]
	ds_read_b64_tr_b16 v[244:245], v205 offset:52224
	ds_read_b64_tr_b16 v[248:249], v205 offset:52256
	ds_read_b64_tr_b16 v[216:217], v205 offset:52288
	ds_read_b64_tr_b16 v[220:221], v205 offset:52320
	ds_read_b64_tr_b16 v[246:247], v206 offset:52224
	ds_read_b64_tr_b16 v[250:251], v206 offset:52256
	ds_read_b64_tr_b16 v[218:219], v206 offset:52288
	ds_read_b64_tr_b16 v[222:223], v206 offset:52320
	v_mfma_f32_16x16x32_bf16 v[36:39], v[184:187], v[212:215], v[36:39]
	v_mfma_f32_16x16x32_bf16 v[32:35], v[188:191], v[212:215], v[32:35]
	s_waitcnt lgkmcnt(3)
	v_mfma_f32_16x16x32_bf16 v[172:175], v[244:247], v[192:195], v[172:175]
	ds_read_b128 v[184:187], v199 offset:41984
	buffer_load_dwordx4 v[24:27], v197, s[24:27], s9 offen
	s_waitcnt vmcnt(12)
	v_cvt_pk_bf16_f32 v15, v14, v15
	v_cvt_pk_bf16_f32 v14, v12, v13
	s_waitcnt lgkmcnt(3)
	v_mfma_f32_16x16x32_bf16 v[168:171], v[248:251], v[192:195], v[168:171]
	ds_write_b64 v198, v[14:15] offset:256
	s_waitcnt lgkmcnt(3)
	v_mfma_f32_16x16x32_bf16 v[164:167], v[216:219], v[192:195], v[164:167]
	s_waitcnt lgkmcnt(2)
	v_mfma_f32_16x16x32_bf16 v[160:163], v[220:223], v[192:195], v[160:163]
	v_mfma_f32_16x16x32_bf16 v[156:159], v[244:247], v[176:179], v[156:159]
	ds_read_b128 v[188:191], v199 offset:44032
	v_mfma_f32_16x16x32_bf16 v[152:155], v[248:251], v[176:179], v[152:155]
	v_mfma_f32_16x16x32_bf16 v[148:151], v[216:219], v[176:179], v[148:151]
	v_mfma_f32_16x16x32_bf16 v[144:147], v[220:223], v[176:179], v[144:147]
	s_waitcnt lgkmcnt(2)
	v_mfma_f32_16x16x32_bf16 v[132:135], v[244:247], v[184:187], v[132:135]
	ds_read_b128 v[176:179], v199 offset:46080
	buffer_load_dwordx4 v[12:15], v197, s[16:19], s38 offen
	s_waitcnt vmcnt(12)
	v_cvt_pk_bf16_f32 v7, v6, v7
	v_cvt_pk_bf16_f32 v6, v4, v5
	v_mfma_f32_16x16x32_bf16 v[124:127], v[248:251], v[184:187], v[124:127]
	ds_write_b64 v198, v[6:7] offset:8960
	v_mfma_f32_16x16x32_bf16 v[120:123], v[216:219], v[184:187], v[120:123]
	v_mfma_f32_16x16x32_bf16 v[140:143], v[220:223], v[184:187], v[140:143]
	s_waitcnt lgkmcnt(2)
	v_mfma_f32_16x16x32_bf16 v[136:139], v[244:247], v[188:191], v[136:139]
	ds_read_b128 v[184:187], v199 offset:48128
	v_mfma_f32_16x16x32_bf16 v[128:131], v[248:251], v[188:191], v[128:131]
	v_mfma_f32_16x16x32_bf16 v[116:119], v[216:219], v[188:191], v[116:119]
	v_mfma_f32_16x16x32_bf16 v[112:115], v[220:223], v[188:191], v[112:115]
	s_waitcnt lgkmcnt(2)
	v_mfma_f32_16x16x32_bf16 v[100:103], v[244:247], v[176:179], v[100:103]
	ds_read_b128 v[188:191], v199 offset:50176
	buffer_load_dwordx4 v[4:7], v197, s[16:19], s39 offen
	s_waitcnt vmcnt(12)
	v_cvt_pk_bf16_f32 v3, v2, v3
	v_cvt_pk_bf16_f32 v2, v0, v1
	v_mfma_f32_16x16x32_bf16 v[92:95], v[248:251], v[176:179], v[92:95]
	ds_write_b64 v198, v[2:3] offset:17664
	v_mfma_f32_16x16x32_bf16 v[88:91], v[216:219], v[176:179], v[88:91]
	v_mfma_f32_16x16x32_bf16 v[108:111], v[220:223], v[176:179], v[108:111]
	s_waitcnt lgkmcnt(2)
	v_mfma_f32_16x16x32_bf16 v[104:107], v[244:247], v[184:187], v[104:107]
	ds_read_b128 v[176:179], v199 offset:52224
	v_mfma_f32_16x16x32_bf16 v[96:99], v[248:251], v[184:187], v[96:99]
	v_mfma_f32_16x16x32_bf16 v[84:87], v[216:219], v[184:187], v[84:87]
	v_mfma_f32_16x16x32_bf16 v[80:83], v[220:223], v[184:187], v[80:83]
	s_waitcnt lgkmcnt(2)
	v_mfma_f32_16x16x32_bf16 v[72:75], v[244:247], v[188:191], v[72:75]
	ds_read_b128 v[252:255], v199 offset:54272
	buffer_load_dwordx4 v[0:3], v197, s[16:19], s43 offen
	s_waitcnt vmcnt(12)
	v_cvt_pk_bf16_f32 v11, v10, v11
	v_cvt_pk_bf16_f32 v10, v8, v9
	v_mfma_f32_16x16x32_bf16 v[64:67], v[248:251], v[188:191], v[64:67]
	ds_write_b64 v198, v[10:11] offset:26368
	v_mfma_f32_16x16x32_bf16 v[60:63], v[216:219], v[188:191], v[60:63]
	v_mfma_f32_16x16x32_bf16 v[76:79], v[220:223], v[188:191], v[76:79]
	s_waitcnt lgkmcnt(2)
	v_mfma_f32_16x16x32_bf16 v[68:71], v[244:247], v[176:179], v[68:71]
	buffer_load_dwordx4 v[8:11], v197, s[16:19], s9 offen
	v_mfma_f32_16x16x32_bf16 v[56:59], v[248:251], v[176:179], v[56:59]
	v_mfma_f32_16x16x32_bf16 v[52:55], v[216:219], v[176:179], v[52:55]
	v_mfma_f32_16x16x32_bf16 v[48:51], v[220:223], v[176:179], v[48:51]
	s_waitcnt lgkmcnt(1)
	s_waitcnt vmcnt(8)
	s_waitcnt lgkmcnt(0)
	s_barrier
	s_add_i32 s8, s8, 2
	s_add_i32 s9, s9, 0x100000
	s_addk_i32 s36, 0x100
	s_cmp_ge_i32 s8, s84
	s_cbranch_scc1 .Lflush_P6
; #define G_ENDTILE(VM) do { asm volatile("s_waitcnt vmcnt(" #VM ")" ::: "memory"); \
;         asm volatile("s_waitcnt lgkmcnt(0)" ::: "memory"); __builtin_amdgcn_s_barrier(); asm volatile("" ::: "memory"); } while (0)
;     ...
;         for (int t = 0; t < nt - 2; t += 2) {
;             G_TILE(G_A0, G_B0, true, G_B1, G_A1, t + 1, true, t + 2, (void)0);
;             G_ENDTILE(8);
;             G_TILE(G_A1, G_B1, true, G_B0, G_A0, t + 2, true, t + 3, (void)0);
;             G_ENDTILE(8);
.LBB0_863:
	s_mov_b32 m0, s85
	s_add_i32 s38, s36, 0xffffff80
	ds_read_b64_tr_b16 v[178:179], v206
	ds_read_b64_tr_b16 v[176:177], v205
	ds_read_b64_tr_b16 v[180:181], v205 offset:32
	ds_read_b64_tr_b16 v[184:185], v205 offset:64
	ds_read_b64_tr_b16 v[188:189], v205 offset:96
	ds_read_b128 v[192:195], v199
	ds_read_b64_tr_b16 v[182:183], v206 offset:32
	ds_read_b64_tr_b16 v[186:187], v206 offset:64
	ds_read_b64_tr_b16 v[190:191], v206 offset:96
	ds_read_b128 v[208:211], v199 offset:2048
	ds_read_b128 v[212:215], v199 offset:4096
	buffer_load_dwordx4 v200, s[20:23], s38 offen lds
	s_mov_b32 m0, s86
	v_mfma_f32_16x16x32_bf16 v[44:47], v[244:247], v[252:255], v[44:47]
	v_mfma_f32_16x16x32_bf16 v[40:43], v[248:251], v[252:255], v[40:43]
	v_mfma_f32_16x16x32_bf16 v[36:39], v[216:219], v[252:255], v[36:39]
	v_mfma_f32_16x16x32_bf16 v[32:35], v[220:223], v[252:255], v[32:35]
	s_waitcnt lgkmcnt(0)
	v_mfma_f32_16x16x32_bf16 v[172:175], v[176:179], v[192:195], v[172:175]
	buffer_load_dwordx4 v201, s[20:23], s38 offen lds
	v_mfma_f32_16x16x32_bf16 v[168:171], v[180:183], v[192:195], v[168:171]
	v_mfma_f32_16x16x32_bf16 v[164:167], v[184:187], v[192:195], v[164:167]
	v_mfma_f32_16x16x32_bf16 v[160:163], v[188:191], v[192:195], v[160:163]
	v_mfma_f32_16x16x32_bf16 v[156:159], v[176:179], v[208:211], v[156:159]
	s_mov_b32 m0, s87
	s_nop 0
	buffer_load_dwordx4 v202, s[20:23], s38 offen lds
	ds_read_b128 v[192:195], v199 offset:6144
	s_waitcnt vmcnt(10)
	v_cvt_pk_bf16_f32 v23, v22, v23
	v_cvt_pk_bf16_f32 v22, v20, v21
	v_mfma_f32_16x16x32_bf16 v[152:155], v[180:183], v[208:211], v[152:155]
	ds_write_b64 v198, v[22:23] offset:34816
	v_mfma_f32_16x16x32_bf16 v[148:151], v[184:187], v[208:211], v[148:151]
	s_mov_b32 m0, s88
	s_nop 0
	buffer_load_dwordx4 v203, s[20:23], s38 offen lds
	v_mfma_f32_16x16x32_bf16 v[144:147], v[188:191], v[208:211], v[144:147]
	v_mfma_f32_16x16x32_bf16 v[132:135], v[176:179], v[212:215], v[132:135]
	s_mov_b32 m0, s89
	s_nop 0
	buffer_load_dwordx4 v204, s[20:23], s38 offen lds
	s_add_i32 s38, s9, 0xfff20000
	ds_read_b128 v[208:211], v199 offset:8192
	v_mfma_f32_16x16x32_bf16 v[124:127], v[180:183], v[212:215], v[124:127]
	v_mfma_f32_16x16x32_bf16 v[120:123], v[184:187], v[212:215], v[120:123]
	v_mfma_f32_16x16x32_bf16 v[140:143], v[188:191], v[212:215], v[140:143]
	s_waitcnt lgkmcnt(2)
	v_mfma_f32_16x16x32_bf16 v[136:139], v[176:179], v[192:195], v[136:139]
	ds_read_b128 v[212:215], v199 offset:10240
	buffer_load_dwordx4 v[20:23], v197, s[24:27], s38 offen
	s_waitcnt vmcnt(11)
	v_cvt_pk_bf16_f32 v31, v30, v31
	v_cvt_pk_bf16_f32 v30, v28, v29
	v_mfma_f32_16x16x32_bf16 v[128:131], v[180:183], v[192:195], v[128:131]
	ds_write_b64 v198, v[30:31] offset:43520
	v_mfma_f32_16x16x32_bf16 v[116:119], v[184:187], v[192:195], v[116:119]
	v_mfma_f32_16x16x32_bf16 v[112:115], v[188:191], v[192:195], v[112:115]
	s_add_i32 s39, s9, 0xfff40000
	s_waitcnt lgkmcnt(2)
	v_mfma_f32_16x16x32_bf16 v[100:103], v[176:179], v[208:211], v[100:103]
	ds_read_b128 v[192:195], v199 offset:12288
	v_mfma_f32_16x16x32_bf16 v[92:95], v[180:183], v[208:211], v[92:95]
	v_mfma_f32_16x16x32_bf16 v[88:91], v[184:187], v[208:211], v[88:91]
	v_mfma_f32_16x16x32_bf16 v[108:111], v[188:191], v[208:211], v[108:111]
	s_waitcnt lgkmcnt(2)
	v_mfma_f32_16x16x32_bf16 v[104:107], v[176:179], v[212:215], v[104:107]
	ds_read_b128 v[208:211], v199 offset:14336
	v_cvt_pk_bf16_f32 v19, v18, v19
	v_cvt_pk_bf16_f32 v18, v16, v17
	v_mfma_f32_16x16x32_bf16 v[96:99], v[180:183], v[212:215], v[96:99]
	ds_write_b64 v198, v[18:19] offset:52224
	v_mfma_f32_16x16x32_bf16 v[84:87], v[184:187], v[212:215], v[84:87]
	v_mfma_f32_16x16x32_bf16 v[80:83], v[188:191], v[212:215], v[80:83]
	s_add_i32 s43, s9, 0xfff60000
	buffer_load_dwordx4 v[28:31], v197, s[24:27], s39 offen
	s_waitcnt lgkmcnt(2)
	v_mfma_f32_16x16x32_bf16 v[72:75], v[176:179], v[192:195], v[72:75]
	ds_read_b128 v[212:215], v199 offset:16384
	v_mfma_f32_16x16x32_bf16 v[64:67], v[180:183], v[192:195], v[64:67]
	v_mfma_f32_16x16x32_bf16 v[60:63], v[184:187], v[192:195], v[60:63]
	v_mfma_f32_16x16x32_bf16 v[76:79], v[188:191], v[192:195], v[76:79]
	s_waitcnt lgkmcnt(2)
	v_mfma_f32_16x16x32_bf16 v[68:71], v[176:179], v[208:211], v[68:71]
	ds_read_b128 v[192:195], v199 offset:1024
	buffer_load_dwordx4 v[16:19], v197, s[24:27], s43 offen
	s_waitcnt vmcnt(12)
	v_cvt_pk_bf16_f32 v27, v26, v27
	v_cvt_pk_bf16_f32 v26, v24, v25
	v_mfma_f32_16x16x32_bf16 v[56:59], v[180:183], v[208:211], v[56:59]
	ds_write_b64 v198, v[26:27] offset:60928
	v_mfma_f32_16x16x32_bf16 v[52:55], v[184:187], v[208:211], v[52:55]
	v_mfma_f32_16x16x32_bf16 v[48:51], v[188:191], v[208:211], v[48:51]
	s_add_i32 s45, s9, 0xfff80000
	ds_read_b128 v[208:211], v199 offset:3072
	s_waitcnt lgkmcnt(3)
	v_mfma_f32_16x16x32_bf16 v[44:47], v[176:179], v[212:215], v[44:47]
	ds_read_b64_tr_b16 v[246:247], v206 offset:17408
	ds_read_b64_tr_b16 v[218:219], v206 offset:17440
	ds_read_b64_tr_b16 v[244:245], v205 offset:17408
	ds_read_b64_tr_b16 v[216:217], v205 offset:17440
	v_mfma_f32_16x16x32_bf16 v[40:43], v[180:183], v[212:215], v[40:43]
	ds_read_b64_tr_b16 v[248:249], v205 offset:17472
	ds_read_b64_tr_b16 v[250:251], v206 offset:17472
	v_mfma_f32_16x16x32_bf16 v[36:39], v[184:187], v[212:215], v[36:39]
	ds_read_b64_tr_b16 v[252:253], v205 offset:17504
	ds_read_b64_tr_b16 v[254:255], v206 offset:17504
	v_mfma_f32_16x16x32_bf16 v[32:35], v[188:191], v[212:215], v[32:35]
	s_waitcnt lgkmcnt(5)
	v_mfma_f32_16x16x32_bf16 v[172:175], v[244:247], v[192:195], v[172:175]
	ds_read_b128 v[188:191], v199 offset:5120
	buffer_load_dwordx4 v[24:27], v197, s[24:27], s45 offen
	s_waitcnt vmcnt(12)
	v_cvt_pk_bf16_f32 v15, v14, v15
	v_cvt_pk_bf16_f32 v14, v12, v13
	s_waitcnt lgkmcnt(5)
	v_mfma_f32_16x16x32_bf16 v[168:171], v[216:219], v[192:195], v[168:171]
	ds_write_b64 v198, v[14:15] offset:35072
	s_waitcnt lgkmcnt(4)
	v_mfma_f32_16x16x32_bf16 v[164:167], v[248:251], v[192:195], v[164:167]
	s_waitcnt lgkmcnt(2)
	v_mfma_f32_16x16x32_bf16 v[160:163], v[252:255], v[192:195], v[160:163]
	v_mfma_f32_16x16x32_bf16 v[156:159], v[244:247], v[208:211], v[156:159]
	ds_read_b128 v[192:195], v199 offset:7168
	v_mfma_f32_16x16x32_bf16 v[152:155], v[216:219], v[208:211], v[152:155]
	v_mfma_f32_16x16x32_bf16 v[148:151], v[248:251], v[208:211], v[148:151]
	v_mfma_f32_16x16x32_bf16 v[144:147], v[252:255], v[208:211], v[144:147]
	s_waitcnt lgkmcnt(2)
	v_mfma_f32_16x16x32_bf16 v[132:135], v[244:247], v[188:191], v[132:135]
	ds_read_b128 v[208:211], v199 offset:9216
	buffer_load_dwordx4 v[12:15], v197, s[16:19], s38 offen
	s_waitcnt vmcnt(11)
	v_cvt_pk_bf16_f32 v7, v6, v7
	v_cvt_pk_bf16_f32 v6, v4, v5
	v_mfma_f32_16x16x32_bf16 v[124:127], v[216:219], v[188:191], v[124:127]
	ds_write_b64 v198, v[6:7] offset:43776
	v_mfma_f32_16x16x32_bf16 v[120:123], v[248:251], v[188:191], v[120:123]
	v_mfma_f32_16x16x32_bf16 v[140:143], v[252:255], v[188:191], v[140:143]
	s_waitcnt lgkmcnt(2)
	v_mfma_f32_16x16x32_bf16 v[136:139], v[244:247], v[192:195], v[136:139]
	ds_read_b128 v[188:191], v199 offset:11264
	v_mfma_f32_16x16x32_bf16 v[128:131], v[216:219], v[192:195], v[128:131]
	v_mfma_f32_16x16x32_bf16 v[116:119], v[248:251], v[192:195], v[116:119]
	v_mfma_f32_16x16x32_bf16 v[112:115], v[252:255], v[192:195], v[112:115]
	s_waitcnt lgkmcnt(2)
	v_mfma_f32_16x16x32_bf16 v[100:103], v[244:247], v[208:211], v[100:103]
	ds_read_b128 v[192:195], v199 offset:13312
	v_cvt_pk_bf16_f32 v3, v2, v3
	v_cvt_pk_bf16_f32 v2, v0, v1
	v_mfma_f32_16x16x32_bf16 v[92:95], v[216:219], v[208:211], v[92:95]
	ds_write_b64 v198, v[2:3] offset:52480
	v_mfma_f32_16x16x32_bf16 v[88:91], v[248:251], v[208:211], v[88:91]
	v_mfma_f32_16x16x32_bf16 v[108:111], v[252:255], v[208:211], v[108:111]
	buffer_load_dwordx4 v[4:7], v197, s[16:19], s39 offen
	s_waitcnt lgkmcnt(2)
	v_mfma_f32_16x16x32_bf16 v[104:107], v[244:247], v[188:191], v[104:107]
	ds_read_b128 v[208:211], v199 offset:15360
	v_mfma_f32_16x16x32_bf16 v[96:99], v[216:219], v[188:191], v[96:99]
	v_mfma_f32_16x16x32_bf16 v[84:87], v[248:251], v[188:191], v[84:87]
	v_mfma_f32_16x16x32_bf16 v[80:83], v[252:255], v[188:191], v[80:83]
	s_waitcnt lgkmcnt(2)
	v_mfma_f32_16x16x32_bf16 v[72:75], v[244:247], v[192:195], v[72:75]
	ds_read_b128 v[236:239], v199 offset:17408
	buffer_load_dwordx4 v[0:3], v197, s[16:19], s43 offen
	s_waitcnt vmcnt(12)
	v_cvt_pk_bf16_f32 v11, v10, v11
	v_cvt_pk_bf16_f32 v10, v8, v9
	v_mfma_f32_16x16x32_bf16 v[64:67], v[216:219], v[192:195], v[64:67]
	ds_write_b64 v198, v[10:11] offset:61184
	v_mfma_f32_16x16x32_bf16 v[60:63], v[248:251], v[192:195], v[60:63]
	v_mfma_f32_16x16x32_bf16 v[76:79], v[252:255], v[192:195], v[76:79]
	s_waitcnt lgkmcnt(2)
	v_mfma_f32_16x16x32_bf16 v[68:71], v[244:247], v[208:211], v[68:71]
	buffer_load_dwordx4 v[8:11], v197, s[16:19], s45 offen
	v_mfma_f32_16x16x32_bf16 v[56:59], v[216:219], v[208:211], v[56:59]
	v_mfma_f32_16x16x32_bf16 v[52:55], v[248:251], v[208:211], v[52:55]
	v_mfma_f32_16x16x32_bf16 v[48:51], v[252:255], v[208:211], v[48:51]
	s_waitcnt lgkmcnt(1)
	s_waitcnt vmcnt(8)
	s_mov_b32 m0, s49
	s_waitcnt lgkmcnt(0)
	s_barrier
	ds_read_b64_tr_b16 v[178:179], v206 offset:34816
	ds_read_b64_tr_b16 v[176:177], v205 offset:34816
	ds_read_b64_tr_b16 v[180:181], v205 offset:34848
	ds_read_b64_tr_b16 v[184:185], v205 offset:34880
	ds_read_b64_tr_b16 v[188:189], v205 offset:34912
	ds_read_b128 v[192:195], v199 offset:36864
	ds_read_b64_tr_b16 v[182:183], v206 offset:34848
	ds_read_b64_tr_b16 v[186:187], v206 offset:34880
	ds_read_b64_tr_b16 v[190:191], v206 offset:34912
	ds_read_b128 v[208:211], v199 offset:38912
	ds_read_b128 v[212:215], v199 offset:40960
	buffer_load_dwordx4 v200, s[20:23], s36 offen lds
	s_mov_b32 m0, s68
	v_mfma_f32_16x16x32_bf16 v[44:47], v[244:247], v[236:239], v[44:47]
	v_mfma_f32_16x16x32_bf16 v[40:43], v[216:219], v[236:239], v[40:43]
	v_mfma_f32_16x16x32_bf16 v[36:39], v[248:251], v[236:239], v[36:39]
	v_mfma_f32_16x16x32_bf16 v[32:35], v[252:255], v[236:239], v[32:35]
	s_waitcnt lgkmcnt(5)
	v_mfma_f32_16x16x32_bf16 v[172:175], v[176:179], v[192:195], v[172:175]
	buffer_load_dwordx4 v201, s[20:23], s36 offen lds
	s_add_i32 s38, s9, 0xfffa0000
	s_waitcnt lgkmcnt(4)
	v_mfma_f32_16x16x32_bf16 v[168:171], v[180:183], v[192:195], v[168:171]
	s_waitcnt lgkmcnt(3)
	v_mfma_f32_16x16x32_bf16 v[164:167], v[184:187], v[192:195], v[164:167]
	s_waitcnt lgkmcnt(2)
	v_mfma_f32_16x16x32_bf16 v[160:163], v[188:191], v[192:195], v[160:163]
	s_waitcnt lgkmcnt(1)
	v_mfma_f32_16x16x32_bf16 v[156:159], v[176:179], v[208:211], v[156:159]
	s_mov_b32 m0, s77
	s_nop 0
	buffer_load_dwordx4 v202, s[20:23], s36 offen lds
	ds_read_b128 v[192:195], v199 offset:43008
	s_waitcnt vmcnt(10)
	v_cvt_pk_bf16_f32 v23, v22, v23
	v_cvt_pk_bf16_f32 v22, v20, v21
	v_mfma_f32_16x16x32_bf16 v[152:155], v[180:183], v[208:211], v[152:155]
	ds_write_b64 v198, v[22:23]
	v_mfma_f32_16x16x32_bf16 v[148:151], v[184:187], v[208:211], v[148:151]
	s_mov_b32 m0, s78
	s_nop 0
	buffer_load_dwordx4 v203, s[20:23], s36 offen lds
	v_mfma_f32_16x16x32_bf16 v[144:147], v[188:191], v[208:211], v[144:147]
	s_waitcnt lgkmcnt(2)
	v_mfma_f32_16x16x32_bf16 v[132:135], v[176:179], v[212:215], v[132:135]
	s_mov_b32 m0, s79
	s_nop 0
	buffer_load_dwordx4 v204, s[20:23], s36 offen lds
	ds_read_b128 v[208:211], v199 offset:45056
	v_mfma_f32_16x16x32_bf16 v[124:127], v[180:183], v[212:215], v[124:127]
	v_mfma_f32_16x16x32_bf16 v[120:123], v[184:187], v[212:215], v[120:123]
	v_mfma_f32_16x16x32_bf16 v[140:143], v[188:191], v[212:215], v[140:143]
	s_waitcnt lgkmcnt(2)
	v_mfma_f32_16x16x32_bf16 v[136:139], v[176:179], v[192:195], v[136:139]
	ds_read_b128 v[212:215], v199 offset:47104
	buffer_load_dwordx4 v[20:23], v197, s[24:27], s38 offen
	s_waitcnt vmcnt(12)
	v_cvt_pk_bf16_f32 v31, v30, v31
	v_cvt_pk_bf16_f32 v30, v28, v29
	v_mfma_f32_16x16x32_bf16 v[128:131], v[180:183], v[192:195], v[128:131]
	ds_write_b64 v198, v[30:31] offset:8704
	v_mfma_f32_16x16x32_bf16 v[116:119], v[184:187], v[192:195], v[116:119]
	v_mfma_f32_16x16x32_bf16 v[112:115], v[188:191], v[192:195], v[112:115]
	s_add_i32 s39, s9, 0xfffc0000
	s_waitcnt lgkmcnt(2)
	v_mfma_f32_16x16x32_bf16 v[100:103], v[176:179], v[208:211], v[100:103]
	ds_read_b128 v[192:195], v199 offset:49152
	v_mfma_f32_16x16x32_bf16 v[92:95], v[180:183], v[208:211], v[92:95]
	v_mfma_f32_16x16x32_bf16 v[88:91], v[184:187], v[208:211], v[88:91]
	v_mfma_f32_16x16x32_bf16 v[108:111], v[188:191], v[208:211], v[108:111]
	s_waitcnt lgkmcnt(2)
	v_mfma_f32_16x16x32_bf16 v[104:107], v[176:179], v[212:215], v[104:107]
	ds_read_b128 v[208:211], v199 offset:51200
	buffer_load_dwordx4 v[28:31], v197, s[24:27], s39 offen
	s_waitcnt vmcnt(12)
	v_cvt_pk_bf16_f32 v19, v18, v19
	v_cvt_pk_bf16_f32 v18, v16, v17
	v_mfma_f32_16x16x32_bf16 v[96:99], v[180:183], v[212:215], v[96:99]
	ds_write_b64 v198, v[18:19] offset:17408
	v_mfma_f32_16x16x32_bf16 v[84:87], v[184:187], v[212:215], v[84:87]
	v_mfma_f32_16x16x32_bf16 v[80:83], v[188:191], v[212:215], v[80:83]
	s_add_i32 s43, s9, 0xfffe0000
	s_waitcnt lgkmcnt(2)
	v_mfma_f32_16x16x32_bf16 v[72:75], v[176:179], v[192:195], v[72:75]
	ds_read_b128 v[212:215], v199 offset:53248
	v_mfma_f32_16x16x32_bf16 v[64:67], v[180:183], v[192:195], v[64:67]
	v_mfma_f32_16x16x32_bf16 v[60:63], v[184:187], v[192:195], v[60:63]
	v_mfma_f32_16x16x32_bf16 v[76:79], v[188:191], v[192:195], v[76:79]
	s_waitcnt lgkmcnt(2)
	v_mfma_f32_16x16x32_bf16 v[68:71], v[176:179], v[208:211], v[68:71]
	ds_read_b128 v[192:195], v199 offset:37888
	buffer_load_dwordx4 v[16:19], v197, s[24:27], s43 offen
	s_waitcnt vmcnt(12)
	v_cvt_pk_bf16_f32 v27, v26, v27
	v_cvt_pk_bf16_f32 v26, v24, v25
	v_mfma_f32_16x16x32_bf16 v[56:59], v[180:183], v[208:211], v[56:59]
	ds_write_b64 v198, v[26:27] offset:26112
	v_mfma_f32_16x16x32_bf16 v[52:55], v[184:187], v[208:211], v[52:55]
	v_mfma_f32_16x16x32_bf16 v[48:51], v[188:191], v[208:211], v[48:51]
	s_waitcnt lgkmcnt(2)
	v_mfma_f32_16x16x32_bf16 v[44:47], v[176:179], v[212:215], v[44:47]
	ds_read_b128 v[176:179], v199 offset:39936
	v_mfma_f32_16x16x32_bf16 v[40:43], v[180:183], v[212:215], v[40:43]
	ds_read_b64_tr_b16 v[244:245], v205 offset:52224
	ds_read_b64_tr_b16 v[248:249], v205 offset:52256
	ds_read_b64_tr_b16 v[216:217], v205 offset:52288
	ds_read_b64_tr_b16 v[220:221], v205 offset:52320
	ds_read_b64_tr_b16 v[246:247], v206 offset:52224
	ds_read_b64_tr_b16 v[250:251], v206 offset:52256
	ds_read_b64_tr_b16 v[218:219], v206 offset:52288
	ds_read_b64_tr_b16 v[222:223], v206 offset:52320
	v_mfma_f32_16x16x32_bf16 v[36:39], v[184:187], v[212:215], v[36:39]
	v_mfma_f32_16x16x32_bf16 v[32:35], v[188:191], v[212:215], v[32:35]
	s_waitcnt lgkmcnt(3)
	v_mfma_f32_16x16x32_bf16 v[172:175], v[244:247], v[192:195], v[172:175]
	ds_read_b128 v[184:187], v199 offset:41984
	buffer_load_dwordx4 v[24:27], v197, s[24:27], s9 offen
	s_waitcnt vmcnt(12)
; #define G_ENDTILE(VM) do { asm volatile("s_waitcnt vmcnt(" #VM ")" ::: "memory"); \
;         asm volatile("s_waitcnt lgkmcnt(0)" ::: "memory"); __builtin_amdgcn_s_barrier(); asm volatile("" ::: "memory"); } while (0)
;     ...
;         for (int t = 0; t < nt - 2; t += 2) {
;             G_TILE(G_A0, G_B0, true, G_B1, G_A1, t + 1, true, t + 2, (void)0);
;             G_ENDTILE(8);
;             G_TILE(G_A1, G_B1, true, G_B0, G_A0, t + 2, true, t + 3, (void)0);
;             G_ENDTILE(8);
	v_cvt_pk_bf16_f32 v15, v14, v15
	v_cvt_pk_bf16_f32 v14, v12, v13
	s_waitcnt lgkmcnt(3)
	v_mfma_f32_16x16x32_bf16 v[168:171], v[248:251], v[192:195], v[168:171]
	ds_write_b64 v198, v[14:15] offset:256
	s_waitcnt lgkmcnt(3)
	v_mfma_f32_16x16x32_bf16 v[164:167], v[216:219], v[192:195], v[164:167]
	s_waitcnt lgkmcnt(2)
	v_mfma_f32_16x16x32_bf16 v[160:163], v[220:223], v[192:195], v[160:163]
	v_mfma_f32_16x16x32_bf16 v[156:159], v[244:247], v[176:179], v[156:159]
	ds_read_b128 v[188:191], v199 offset:44032
	v_mfma_f32_16x16x32_bf16 v[152:155], v[248:251], v[176:179], v[152:155]
	v_mfma_f32_16x16x32_bf16 v[148:151], v[216:219], v[176:179], v[148:151]
	v_mfma_f32_16x16x32_bf16 v[144:147], v[220:223], v[176:179], v[144:147]
	s_waitcnt lgkmcnt(2)
	v_mfma_f32_16x16x32_bf16 v[132:135], v[244:247], v[184:187], v[132:135]
	ds_read_b128 v[176:179], v199 offset:46080
	buffer_load_dwordx4 v[12:15], v197, s[16:19], s38 offen
	s_waitcnt vmcnt(12)
	v_cvt_pk_bf16_f32 v7, v6, v7
	v_cvt_pk_bf16_f32 v6, v4, v5
	v_mfma_f32_16x16x32_bf16 v[124:127], v[248:251], v[184:187], v[124:127]
	ds_write_b64 v198, v[6:7] offset:8960
	v_mfma_f32_16x16x32_bf16 v[120:123], v[216:219], v[184:187], v[120:123]
	v_mfma_f32_16x16x32_bf16 v[140:143], v[220:223], v[184:187], v[140:143]
	s_waitcnt lgkmcnt(2)
	v_mfma_f32_16x16x32_bf16 v[136:139], v[244:247], v[188:191], v[136:139]
	ds_read_b128 v[184:187], v199 offset:48128
	v_mfma_f32_16x16x32_bf16 v[128:131], v[248:251], v[188:191], v[128:131]
	v_mfma_f32_16x16x32_bf16 v[116:119], v[216:219], v[188:191], v[116:119]
	v_mfma_f32_16x16x32_bf16 v[112:115], v[220:223], v[188:191], v[112:115]
	s_waitcnt lgkmcnt(2)
	v_mfma_f32_16x16x32_bf16 v[100:103], v[244:247], v[176:179], v[100:103]
	ds_read_b128 v[188:191], v199 offset:50176
	buffer_load_dwordx4 v[4:7], v197, s[16:19], s39 offen
	s_waitcnt vmcnt(12)
	v_cvt_pk_bf16_f32 v3, v2, v3
	v_cvt_pk_bf16_f32 v2, v0, v1
	v_mfma_f32_16x16x32_bf16 v[92:95], v[248:251], v[176:179], v[92:95]
	ds_write_b64 v198, v[2:3] offset:17664
	v_mfma_f32_16x16x32_bf16 v[88:91], v[216:219], v[176:179], v[88:91]
	v_mfma_f32_16x16x32_bf16 v[108:111], v[220:223], v[176:179], v[108:111]
	s_waitcnt lgkmcnt(2)
	v_mfma_f32_16x16x32_bf16 v[104:107], v[244:247], v[184:187], v[104:107]
	ds_read_b128 v[176:179], v199 offset:52224
	v_mfma_f32_16x16x32_bf16 v[96:99], v[248:251], v[184:187], v[96:99]
	v_mfma_f32_16x16x32_bf16 v[84:87], v[216:219], v[184:187], v[84:87]
	v_mfma_f32_16x16x32_bf16 v[80:83], v[220:223], v[184:187], v[80:83]
	s_waitcnt lgkmcnt(2)
	v_mfma_f32_16x16x32_bf16 v[72:75], v[244:247], v[188:191], v[72:75]
	ds_read_b128 v[252:255], v199 offset:54272
	buffer_load_dwordx4 v[0:3], v197, s[16:19], s43 offen
	s_waitcnt vmcnt(12)
	v_cvt_pk_bf16_f32 v11, v10, v11
	v_cvt_pk_bf16_f32 v10, v8, v9
	v_mfma_f32_16x16x32_bf16 v[64:67], v[248:251], v[188:191], v[64:67]
	ds_write_b64 v198, v[10:11] offset:26368
	v_mfma_f32_16x16x32_bf16 v[60:63], v[216:219], v[188:191], v[60:63]
	v_mfma_f32_16x16x32_bf16 v[76:79], v[220:223], v[188:191], v[76:79]
	s_waitcnt lgkmcnt(2)
	v_mfma_f32_16x16x32_bf16 v[68:71], v[244:247], v[176:179], v[68:71]
	buffer_load_dwordx4 v[8:11], v197, s[16:19], s9 offen
	v_mfma_f32_16x16x32_bf16 v[56:59], v[248:251], v[176:179], v[56:59]
	v_mfma_f32_16x16x32_bf16 v[52:55], v[216:219], v[176:179], v[52:55]
	v_mfma_f32_16x16x32_bf16 v[48:51], v[220:223], v[176:179], v[48:51]
	s_waitcnt lgkmcnt(1)
	s_waitcnt vmcnt(8)
	s_waitcnt lgkmcnt(0)
	s_barrier
	s_add_i32 s8, s8, 2
	s_add_i32 s9, s9, 0x100000
	s_addk_i32 s36, 0x100
	s_cmp_ge_i32 s8, s84
	s_cbranch_scc0 .LBB0_863
